# expert-phase cleanups: batched per-wave init loads, one-op gather addresses in the u loop, interleaved MFMA/stage/loads in the v loop
# speedup vs baseline: 1.0479x; 1.0056x over previous
; #define GAS __attribute__((address_space(1)))
; #define LAS __attribute__((address_space(3)))
; #define LDS_WAIT() asm volatile("s_waitcnt lgkmcnt(0)" ::: "memory")
; __device__ __forceinline__ float frsq(float x) { return __builtin_amdgcn_rsqf(x); }
; #define XFENCE() asm volatile("" ::: "memory")
; __device__ __forceinline__ void expert_phase(const Frame& F, int l, int xcc, LAS unsigned char* wl, const LAS unsigned char* zb) {
;     ...
;             float zf = 0.f; asm volatile("" : "+v"(zf)); const f32x4 z = (f32x4){zf, zf, zf, zf};
; #pragma unroll
;             for (int i = 0; i < 8; ++i) *(LAS f32x4*)(SA + (i * 64 + lane) * 4) = z;
; #pragma unroll
;             for (int i = 0; i < 2; ++i) *(LAS f32x4*)(SQ + (i * 64 + lane) * 4) = z;
; #pragma unroll
;             for (int k = 0; k < 8; ++k) { const u32x2 e2 = ldo_u2(EXPI + (size_t)tok(k) * 128, 8u * lane); *(LAS unsigned*)(IDL + k * 256 + lane * 4) = e2.x | (e2.y << 16); }
;             const float* SS2 = (const float*)(F.ws + WS_SS2);
;             float ss[8];
; #pragma unroll
;             for (int k = 0; k < 8; ++k) ss[k] = *(const GAS float*)(SS2 + (size_t)(lane & 31) * T + tok(k));
; #pragma unroll
;             for (int k = 0; k < 8; ++k) { const float tot = wave_sum(ss[k]) * 0.5f; if (lane == 0) RS[k] = frsq(tot * (1.f / D) + EPS); }
;             LDS_WAIT(); XFENCE();
.LBB0_1125:
	v_mov_b32_e32 v0, v185
	s_ashr_i32 s27, s26, 31
	v_add_u32_e32 v4, s83, v182
	s_waitcnt lgkmcnt(0)
	v_mov_b32_e32 v1, v0
	v_mov_b32_e32 v2, v0
	v_mov_b32_e32 v3, v0
	s_lshl_b64 s[2:3], s[26:27], 9
	ds_write_b128 v4, v[0:3]
	ds_write_b128 v4, v[0:3] offset:1024
	ds_write_b128 v4, v[0:3] offset:2048
	ds_write_b128 v4, v[0:3] offset:3072
	ds_write_b128 v4, v[0:3] offset:4096
	ds_write_b128 v4, v[0:3] offset:5120
	ds_write_b128 v4, v[0:3] offset:6144
	ds_write_b128 v4, v[0:3] offset:7168
	ds_write_b128 v4, v[0:3] offset:8192
	ds_write_b128 v4, v[0:3] offset:9216
	v_lshl_add_u64 v[0:1], v[168:169], 0, s[2:3]
	global_load_dwordx2 v[10:11], v[0:1], off
	s_add_i32 s0, s26, s82
	s_cmpk_lt_i32 s0, 0x4000
	s_cselect_b32 s88, s0, s26
	s_ashr_i32 s89, s88, 31
	s_lshl_b64 s[86:87], s[88:89], 9
	s_add_i32 s4, s0, s82
	s_cmpk_lt_i32 s4, 0x4000
	s_cselect_b32 s0, s4, s26
	s_ashr_i32 s1, s0, 31
	v_add_u32_e32 v3, 64, v201
	s_lshl_b64 s[68:69], s[0:1], 9
	s_add_i32 s4, s4, s82
	s_cmpk_lt_i32 s4, 0x4000
	s_cselect_b32 s16, s4, s26
	s_ashr_i32 s17, s16, 31
	s_lshl_b64 s[80:81], s[16:17], 9
	s_add_i32 s4, s4, s82
	s_cmpk_lt_i32 s4, 0x4000
	s_cselect_b32 s14, s4, s26
	s_ashr_i32 s15, s14, 31
	s_lshl_b64 s[8:9], s[14:15], 9
	s_add_i32 s4, s4, s82
	s_cmpk_lt_i32 s4, 0x4000
	s_cselect_b32 s12, s4, s26
	s_ashr_i32 s13, s12, 31
	s_lshl_b64 s[66:67], s[12:13], 9
	s_add_i32 s4, s4, s82
	s_cmpk_lt_i32 s4, 0x4000
	s_cselect_b32 s94, s4, s26
	s_ashr_i32 s95, s94, 31
	s_lshl_b64 s[30:31], s[94:95], 9
	s_add_i32 s4, s4, s82
	s_cmpk_lt_i32 s4, 0x4000
	s_cselect_b32 s6, s4, s26
	s_ashr_i32 s7, s6, 31
	s_lshl_b64 s[44:45], s[6:7], 9
	v_lshl_add_u64 v[8:9], s[6:7], 2, v[166:167]
	v_lshl_add_u64 v[0:1], v[168:169], 0, s[86:87]
	global_load_dwordx2 v[12:13], v[0:1], off
	v_lshl_add_u64 v[0:1], v[168:169], 0, s[68:69]
	global_load_dwordx2 v[14:15], v[0:1], off
	v_lshl_add_u64 v[0:1], v[168:169], 0, s[80:81]
	global_load_dwordx2 v[16:17], v[0:1], off
	v_lshl_add_u64 v[0:1], v[168:169], 0, s[8:9]
	global_load_dwordx2 v[18:19], v[0:1], off
	v_lshl_add_u64 v[0:1], v[168:169], 0, s[66:67]
	global_load_dwordx2 v[20:21], v[0:1], off
	v_lshl_add_u64 v[0:1], v[168:169], 0, s[30:31]
	global_load_dwordx2 v[22:23], v[0:1], off
	v_lshl_add_u64 v[0:1], v[168:169], 0, s[44:45]
	global_load_dwordx2 v[24:25], v[0:1], off
	s_waitcnt vmcnt(0)
	v_lshl_or_b32 v2, v11, 16, v10
	v_lshl_or_b32 v0, v13, 16, v12
	ds_write2st64_b32 v3, v2, v0 offset0:42 offset1:43
	v_lshl_or_b32 v2, v15, 16, v14
	v_lshl_or_b32 v0, v17, 16, v16
	ds_write2st64_b32 v3, v2, v0 offset0:44 offset1:45
	v_lshl_or_b32 v2, v19, 16, v18
	v_lshl_or_b32 v0, v21, 16, v20
	ds_write2st64_b32 v3, v2, v0 offset0:46 offset1:47
	v_lshl_or_b32 v2, v23, 16, v22
	v_lshl_or_b32 v0, v25, 16, v24
	ds_write2st64_b32 v3, v2, v0 offset0:48 offset1:49
	v_lshl_add_u64 v[0:1], s[26:27], 2, v[166:167]
	global_load_dword v7, v[0:1], off
	v_lshl_add_u64 v[0:1], s[88:89], 2, v[166:167]
	global_load_dword v6, v[0:1], off
	v_lshl_add_u64 v[0:1], s[0:1], 2, v[166:167]
	global_load_dword v5, v[0:1], off
	v_lshl_add_u64 v[0:1], s[16:17], 2, v[166:167]
	global_load_dword v4, v[0:1], off
	v_lshl_add_u64 v[0:1], s[14:15], 2, v[166:167]
	global_load_dword v3, v[0:1], off
	v_lshl_add_u64 v[0:1], s[12:13], 2, v[166:167]
	global_load_dword v2, v[0:1], off
	v_lshl_add_u64 v[0:1], s[94:95], 2, v[166:167]
	global_load_dword v1, v[0:1], off
	s_nop 0
	global_load_dword v0, v[8:9], off
	s_waitcnt vmcnt(7)
	ds_bpermute_b32 v8, v176, v7
	s_waitcnt lgkmcnt(0)
	v_add_f32_e32 v7, v7, v8
	ds_bpermute_b32 v8, v177, v7
	s_waitcnt lgkmcnt(0)
	v_add_f32_e32 v7, v7, v8
	ds_bpermute_b32 v8, v178, v7
	s_waitcnt lgkmcnt(0)
	v_add_f32_e32 v7, v7, v8
	ds_bpermute_b32 v8, v179, v7
	s_waitcnt lgkmcnt(0)
	v_add_f32_e32 v7, v7, v8
	ds_bpermute_b32 v8, v180, v7
	s_waitcnt lgkmcnt(0)
	v_add_f32_e32 v7, v7, v8
	ds_bpermute_b32 v8, v181, v7
	s_and_saveexec_b64 s[64:65], s[34:35]
	s_cbranch_execz .LBB0_1127
	s_waitcnt lgkmcnt(0)
	v_add_f32_e32 v7, v7, v8
	v_mul_f32_e32 v7, 0.5, v7
	v_fmamk_f32 v7, v7, 0x3a000000, v214
	v_rsq_f32_e32 v7, v7
	v_mov_b32_e32 v8, s83
	ds_write_b32 v8, v7 offset:10240

; #define LAS __attribute__((address_space(3)))
; #define XFENCE() asm volatile("" ::: "memory")
; __device__ __forceinline__ void expert_phase(const Frame& F, int l, int xcc, LAS unsigned char* wl, const LAS unsigned char* zb) {
;     ...
;             auto u_x = [&](int i) { return ldo_u2(X1 + (size_t)tok(i & 7) * D + slice_of(i) * 256, 8u * lane); };
;             struct HRows { u32x4 r[8]; };
;             auto u_rows_h = [&](int hs, HRows& H) {
;                 const int i = hs >> 1, mg = hs & 1;
;                 const unsigned char* Usl = UBl + (size_t)slice_of(i) * XSL_BYTES;
;                 const u32x2 id = *(const LAS u32x2*)(IDL + (i & 7) * 256 + c * 16 + mg * 8);
;     ...
;                 const unsigned pm = (U_REP > 1 && urep == 0) ? (unsigned)(U_PROBE_MASK) : 0xffffu;
;     ...
;                 const unsigned pm = 0xffffu;
;     ...
;                 const unsigned i0 = id.x, i1 = id.y;
; #pragma unroll
;                 for (int mm = 0; mm < 4; ++mm) { const unsigned w = mm < 2 ? i0 : i1; const unsigned e = (mm & 1) ? (w >> 16) : (w & 0xffffu); const unsigned off = (e & pm) * 128u + 16u * rq;
;                     H.r[2 * mm] = ldo_u4(Usl, off); H.r[2 * mm + 1] = ldo_u4(Usl + 64, off); }
;             };
;     ...
;             HRows H0, H1, H2, H3;
;             u32x2 xe, xo;
;             xe = u_x(0);
;             u_rows_h(0, H0); u_rows_h(1, H1); u_rows_h(2, H2);
;             xo = u_x(1);
;             XFENCE();
.LBB0_1141:
	s_or_b64 exec, exec, s[64:65]
	s_waitcnt lgkmcnt(0)
	s_mov_b32 s100, 0xcccccccc
	s_mov_b32 s101, 0xcccccccc
	s_movk_i32 s5, 0x80
	v_and_b32_e32 v128, 15, v211
	v_lshrrev_b32_e32 v129, 4, v211
	v_lshrrev_b32_e32 v130, 2, v128
	v_lshrrev_b32_e32 v131, 1, v129
	v_lshl_add_u32 v130, v130, 1, v131
	v_lshlrev_b32_e32 v240, 5, v130
	v_add_u32_e32 v240, s83, v240
	v_add_u32_e32 v240, 0x2a40, v240
	v_and_b32_e32 v130, 3, v128
	v_and_b32_e32 v132, 1, v129
	v_lshl_add_u32 v133, v132, 2, v130
	v_lshlrev_b32_e32 v241, 4, v133
	v_and_b32_e32 v133, 1, v130
	v_lshl_add_u32 v133, v133, 1, v132
	v_lshlrev_b32_e32 v133, 5, v133
	v_lshl_add_u32 v133, v131, 8, v133
	v_lshrrev_b32_e32 v134, 3, v128
	v_lshl_add_u32 v133, v134, 7, v133
	v_lshrrev_b32_e32 v135, 1, v130
	v_lshl_add_u32 v133, v135, 4, v133
	v_add_u32_e32 v133, s83, v133
	v_add_u32_e32 v133, 0x2840, v133
	v_bfe_u32 v135, v128, 2, 1
	v_cmp_eq_u32_e32 vcc, 0, v135
	v_mov_b32_e32 v131, 0x1a000
	s_nop 1
	v_cndmask_b32_e32 v242, v131, v133, vcc
	v_cndmask_b32_e32 v249, v133, v131, vcc
	v_lshl_add_u32 v133, v129, 1, v135
	v_lshlrev_b32_e32 v133, 3, v133
	v_lshl_add_u32 v133, v134, 6, v133
	v_lshl_add_u32 v133, v130, 7, v133
	v_add_u32_e32 v243, s83, v133
	s_mov_b32 vcc_lo, 0xaaaaaaaa
	s_mov_b32 vcc_hi, 0xaaaaaaaa
	s_mov_b32 s77, -2
	s_add_i32 s33, s77, 2
	s_min_i32 s33, s33, 63
	s_lshr_b32 s58, s33, 3
	s_add_i32 s58, s58, s96
	s_and_b32 s58, s58, 7
	s_and_b32 s33, s33, 7
	s_lshl_b32 s78, s58, 21
	s_add_u32 s64, s53, s78
	s_addc_u32 s65, s56, 0
	s_mul_i32 s78, s33, s82
	s_add_i32 s78, s78, s26
	s_cmpk_lt_i32 s78, 0x4000
	s_cselect_b32 s78, s78, s26
	s_ashr_i32 s55, s78, 31
	s_mov_b32 s54, s78
	s_lshl_b64 s[54:55], s[54:55], 12
	s_add_u32 s54, s90, s54
	s_addc_u32 s55, s91, s55
	s_lshl_b32 s78, s58, 9
	s_add_u32 s54, s54, s78
	s_addc_u32 s55, s55, 0
	v_lshl_add_u64 v[208:209], s[54:55], 0, v[184:185]
	global_load_dwordx2 v[172:173], v[208:209], off
	s_lshl_b32 s78, s33, 8
	v_add_u32_e32 v248, s78, v240
	ds_read_b128 v[236:239], v248 offset:0
	s_waitcnt lgkmcnt(0)
	v_mad_u32_u16 v208, v236, s5, v241 op_sel:[0,0,0,0]
	global_load_dwordx4 v[0:3], v208, s[64:65]
	v_mad_u32_u16 v209, v236, s5, v241 op_sel:[1,0,0,0]
	global_load_dwordx4 v[4:7], v209, s[64:65]
	v_mad_u32_u16 v208, v237, s5, v241 op_sel:[0,0,0,0]
	global_load_dwordx4 v[8:11], v208, s[64:65]
	v_mad_u32_u16 v209, v237, s5, v241 op_sel:[1,0,0,0]
	global_load_dwordx4 v[12:15], v209, s[64:65]
	v_mad_u32_u16 v208, v238, s5, v241 op_sel:[0,0,0,0]
	global_load_dwordx4 v[16:19], v208, s[64:65]
	v_mad_u32_u16 v209, v238, s5, v241 op_sel:[1,0,0,0]
	global_load_dwordx4 v[20:23], v209, s[64:65]
	v_mad_u32_u16 v208, v239, s5, v241 op_sel:[0,0,0,0]
	global_load_dwordx4 v[24:27], v208, s[64:65]
	v_mad_u32_u16 v209, v239, s5, v241 op_sel:[1,0,0,0]
	global_load_dwordx4 v[28:31], v209, s[64:65]
	s_lshl_b32 s78, s33, 8
	v_add_u32_e32 v248, s78, v240
	ds_read_b128 v[236:239], v248 offset:16
	s_waitcnt lgkmcnt(0)
	v_mad_u32_u16 v208, v236, s5, v241 op_sel:[0,0,0,0]
	global_load_dwordx4 v[32:35], v208, s[64:65]
	v_mad_u32_u16 v209, v236, s5, v241 op_sel:[1,0,0,0]
	global_load_dwordx4 v[36:39], v209, s[64:65]
	v_mad_u32_u16 v208, v237, s5, v241 op_sel:[0,0,0,0]
	global_load_dwordx4 v[40:43], v208, s[64:65]
	v_mad_u32_u16 v209, v237, s5, v241 op_sel:[1,0,0,0]
	global_load_dwordx4 v[44:47], v209, s[64:65]
	v_mad_u32_u16 v208, v238, s5, v241 op_sel:[0,0,0,0]
	global_load_dwordx4 v[48:51], v208, s[64:65]
	v_mad_u32_u16 v209, v238, s5, v241 op_sel:[1,0,0,0]
	global_load_dwordx4 v[52:55], v209, s[64:65]
	v_mad_u32_u16 v208, v239, s5, v241 op_sel:[0,0,0,0]
	global_load_dwordx4 v[56:59], v208, s[64:65]
	v_mad_u32_u16 v209, v239, s5, v241 op_sel:[1,0,0,0]
	global_load_dwordx4 v[60:63], v209, s[64:65]
	s_mov_b32 s77, -1
	s_add_i32 s33, s77, 2
	s_min_i32 s33, s33, 63
	s_lshr_b32 s58, s33, 3
	s_add_i32 s58, s58, s96
	s_and_b32 s58, s58, 7
	s_and_b32 s33, s33, 7
	s_lshl_b32 s78, s58, 21
	s_add_u32 s64, s53, s78
	s_addc_u32 s65, s56, 0
	s_mul_i32 s78, s33, s82
	s_add_i32 s78, s78, s26
	s_cmpk_lt_i32 s78, 0x4000
	s_cselect_b32 s78, s78, s26
	s_ashr_i32 s55, s78, 31
	s_mov_b32 s54, s78
	s_lshl_b64 s[54:55], s[54:55], 12
	s_add_u32 s54, s90, s54
	s_addc_u32 s55, s91, s55
	s_lshl_b32 s78, s58, 9
	s_add_u32 s54, s54, s78
	s_addc_u32 s55, s55, 0
	v_lshl_add_u64 v[208:209], s[54:55], 0, v[184:185]
	global_load_dwordx2 v[174:175], v[208:209], off
	s_lshl_b32 s78, s33, 8
	v_add_u32_e32 v248, s78, v240
	ds_read_b128 v[236:239], v248 offset:0
	s_waitcnt lgkmcnt(0)
	v_mad_u32_u16 v208, v236, s5, v241 op_sel:[0,0,0,0]
	global_load_dwordx4 v[64:67], v208, s[64:65]
	v_mad_u32_u16 v209, v236, s5, v241 op_sel:[1,0,0,0]
	global_load_dwordx4 v[68:71], v209, s[64:65]
	v_mad_u32_u16 v208, v237, s5, v241 op_sel:[0,0,0,0]
	global_load_dwordx4 v[72:75], v208, s[64:65]
	v_mad_u32_u16 v209, v237, s5, v241 op_sel:[1,0,0,0]
	global_load_dwordx4 v[76:79], v209, s[64:65]
	v_mad_u32_u16 v208, v238, s5, v241 op_sel:[0,0,0,0]
	global_load_dwordx4 v[80:83], v208, s[64:65]
	v_mad_u32_u16 v209, v238, s5, v241 op_sel:[1,0,0,0]
	global_load_dwordx4 v[84:87], v209, s[64:65]
	v_mad_u32_u16 v208, v239, s5, v241 op_sel:[0,0,0,0]
	global_load_dwordx4 v[88:91], v208, s[64:65]
	v_mad_u32_u16 v209, v239, s5, v241 op_sel:[1,0,0,0]
	global_load_dwordx4 v[92:95], v209, s[64:65]
	s_lshl_b32 s78, s33, 8
	v_add_u32_e32 v248, s78, v240
	ds_read_b128 v[236:239], v248 offset:16
	s_waitcnt lgkmcnt(0)
	v_mad_u32_u16 v208, v236, s5, v241 op_sel:[0,0,0,0]
	global_load_dwordx4 v[96:99], v208, s[64:65]
	v_mad_u32_u16 v209, v236, s5, v241 op_sel:[1,0,0,0]
	global_load_dwordx4 v[100:103], v209, s[64:65]
	v_mad_u32_u16 v208, v237, s5, v241 op_sel:[0,0,0,0]
	global_load_dwordx4 v[104:107], v208, s[64:65]
	v_mad_u32_u16 v209, v237, s5, v241 op_sel:[1,0,0,0]
	global_load_dwordx4 v[108:111], v209, s[64:65]
	v_mad_u32_u16 v208, v238, s5, v241 op_sel:[0,0,0,0]
	global_load_dwordx4 v[112:115], v208, s[64:65]
	v_mad_u32_u16 v209, v238, s5, v241 op_sel:[1,0,0,0]
	global_load_dwordx4 v[116:119], v209, s[64:65]
	v_mad_u32_u16 v208, v239, s5, v241 op_sel:[0,0,0,0]
	global_load_dwordx4 v[120:123], v208, s[64:65]
	v_mad_u32_u16 v209, v239, s5, v241 op_sel:[1,0,0,0]
	global_load_dwordx4 v[124:127], v209, s[64:65]
	s_mov_b32 s77, 0
; #define LAS __attribute__((address_space(3)))
; __device__ __forceinline__ void expert_phase(const Frame& F, int l, int xcc, LAS unsigned char* wl, const LAS unsigned char* zb) {
;     ...
;             auto u_bbuild = [&](int i, const u32x2& xw) {
;                 const int k = i & 7;
;                 const f32x4 gg = *(const LAS f32x4*)(G2 + slice_of(i) * 256 + 4 * lane);
;                 const float rstd = RS[k];
;                 const float h0 = bf_lo(xw.x) * rstd * gg[0], h1 = bf_hi(xw.x) * rstd * gg[1], h2 = bf_lo(xw.y) * rstd * gg[2], h3 = bf_hi(xw.y) * rstd * gg[3];
;                 int w = __builtin_amdgcn_cvt_pk_fp8_f32(h0, h1, 0, false); w = __builtin_amdgcn_cvt_pk_fp8_f32(h2, h3, w, true);
;                 const f32x2 b0 = __builtin_amdgcn_cvt_pk_f32_fp8(w, false), b1 = __builtin_amdgcn_cvt_pk_f32_fp8(w, true);
;                 int v = __builtin_amdgcn_cvt_pk_fp8_f32(h0 - b0[0], h1 - b0[1], 0, false); v = __builtin_amdgcn_cvt_pk_fp8_f32(h2 - b1[0], h3 - b1[1], v, true);
;                 *(LAS int*)(bw) = w; *(LAS int*)(bw + 128) = v;
;                 LDS_WAIT(); XFENCE();
;                 const u32x4 b0l = *(const LAS u32x4*)(bbase), b0h = *(const LAS u32x4*)(bbase + 16), b1l = *(const LAS u32x4*)(bbase + 256), b1h = *(const LAS u32x4*)(bbase + 272);
;                 B0 = (i32x8){(int)b0l.x, (int)b0l.y, (int)b0l.z, (int)b0l.w, (int)b0h.x, (int)b0h.y, (int)b0h.z, (int)b0h.w};
;                 B1 = (i32x8){(int)b1l.x, (int)b1l.y, (int)b1l.z, (int)b1l.w, (int)b1h.x, (int)b1h.y, (int)b1h.z, (int)b1h.w};
;             };
;             auto u_comp_h = [&](int hs, HRows& H) {
;                 const int k = (hs >> 1) & 7, mg = hs & 1;
;                 LAS f32x4* tp = (LAS f32x4*)(SA + k * 256 + (c & 1) * 16 + 4 * rq) + mg * 32;
;                 f32x4 acc[4];
; #pragma unroll
;                 for (int mm = 0; mm < 4; ++mm) acc[mm] = (f32x4){0.f, 0.f, 0.f, 0.f};
;                 if (c < 2) {
; #pragma unroll
;                     for (int mm = 0; mm < 4; ++mm) acc[mm] = tp[mm * 8];
;                 }
; #pragma unroll
;                 for (int mm = 0; mm < 4; ++mm) {
;                     const i32x8 a0 = {(int)H.r[2 * mm].x, (int)H.r[2 * mm].y, (int)H.r[2 * mm].z, (int)H.r[2 * mm].w, 0, 0, 0, 0};
;                     const i32x8 a1 = {(int)H.r[2 * mm + 1].x, (int)H.r[2 * mm + 1].y, (int)H.r[2 * mm + 1].z, (int)H.r[2 * mm + 1].w, 0, 0, 0, 0};
.Lu_loop:
	s_and_b32 s4, s77, 7
	s_lshl_b32 s78, s4, 2
	s_add_i32 s78, s78, s83
	v_mov_b32_e32 v152, s78
	s_lshr_b32 s78, s77, 3
	s_add_i32 s78, s78, s96
	s_and_b32 s78, s78, 7
	s_lshl_b32 s78, s78, 10
	v_add_u32_e32 v153, s78, v197
	ds_read_b32 v128, v152 offset:10240
	ds_read_b128 v[132:135], v153
	s_lshl_b32 s78, s4, 10
	s_add_i32 s78, s78, s83
	v_add_u32_e32 v210, s78, v184
	s_waitcnt vmcnt(33)
	v_lshlrev_b32_e32 v140, 16, v172
	v_and_b32_e32 v141, 0xffff0000, v172
	v_lshlrev_b32_e32 v142, 16, v173
	v_and_b32_e32 v143, 0xffff0000, v173
	v_mov_b32_e32 v144, 0
	v_mov_b32_e32 v145, 0
	s_waitcnt lgkmcnt(1)
	v_mul_f32_e32 v136, v128, v140
	v_mul_f32_e32 v137, v128, v141
	v_mul_f32_e32 v138, v128, v142
	v_mul_f32_e32 v139, v128, v143
	s_waitcnt lgkmcnt(0)
	v_mul_f32_e32 v140, v132, v136
	v_mul_f32_e32 v141, v133, v137
	v_mul_f32_e32 v142, v134, v138
	v_mul_f32_e32 v143, v135, v139
	v_cvt_pk_fp8_f32 v144, v140, v141
	s_nop 0
	v_cvt_pk_fp8_f32 v144, v142, v143 op_sel:[0,0,1]
	s_nop 0
	v_cvt_pk_f32_fp8_e32 v[148:149], v144
	v_cvt_pk_f32_fp8_sdwa v[150:151], v144 src0_sel:WORD_1
	s_nop 0
	v_fma_f32 v140, v132, v136, -v148
	v_fma_f32 v141, v133, v137, -v149
	v_fma_f32 v142, v134, v138, -v150
	v_fma_f32 v143, v135, v139, -v151
	v_cvt_pk_fp8_f32 v145, v140, v141
	s_nop 0
	v_cvt_pk_fp8_f32 v145, v142, v143 op_sel:[0,0,1]
	v_add_u32_e32 v154, 0x2800, v207
	s_nop 0
	ds_write2_b32 v154, v144, v145 offset0:16 offset1:48
	s_waitcnt lgkmcnt(0)
	ds_read_b128 v[228:231], v242
	ds_read_b128 v[232:235], v249
	s_add_i32 s33, s77, 2
	s_min_i32 s33, s33, 63
	s_lshr_b32 s58, s33, 3
	s_add_i32 s58, s58, s96
	s_and_b32 s58, s58, 7
	s_and_b32 s33, s33, 7
	s_lshl_b32 s78, s58, 21
	s_add_u32 s64, s53, s78
	s_addc_u32 s65, s56, 0
	s_mul_i32 s78, s33, s82
	s_add_i32 s78, s78, s26
	s_cmpk_lt_i32 s78, 0x4000
	s_cselect_b32 s78, s78, s26
	s_ashr_i32 s55, s78, 31
	s_mov_b32 s54, s78
	s_lshl_b64 s[54:55], s[54:55], 12
	s_add_u32 s54, s90, s54
	s_addc_u32 s55, s91, s55
	s_lshl_b32 s78, s58, 9
	s_add_u32 s54, s54, s78
	s_addc_u32 s55, s55, 0
	v_lshl_add_u64 v[208:209], s[54:55], 0, v[184:185]
	global_load_dwordx2 v[172:173], v[208:209], off
	ds_read_b64 v[246:247], v210 offset:0
	s_waitcnt vmcnt(26) lgkmcnt(1)
	v_mfma_scale_f32_16x16x128_f8f6f4 v[128:131], v[0:3], v[228:235], 0, v215, v215 op_sel_hi:[0,0,0] cbsz:4
	v_mfma_scale_f32_16x16x128_f8f6f4 v[132:135], v[4:7], v[228:235], 0, v215, v215 op_sel_hi:[0,0,0] cbsz:4
	v_mfma_scale_f32_16x16x128_f8f6f4 v[136:139], v[8:11], v[228:235], 0, v215, v215 op_sel_hi:[0,0,0] cbsz:4
	v_mfma_scale_f32_16x16x128_f8f6f4 v[140:143], v[12:15], v[228:235], 0, v215, v215 op_sel_hi:[0,0,0] cbsz:4
	v_mfma_scale_f32_16x16x128_f8f6f4 v[144:147], v[16:19], v[228:235], 0, v215, v215 op_sel_hi:[0,0,0] cbsz:4
	v_mfma_scale_f32_16x16x128_f8f6f4 v[148:151], v[20:23], v[228:235], 0, v215, v215 op_sel_hi:[0,0,0] cbsz:4
	v_mfma_scale_f32_16x16x128_f8f6f4 v[152:155], v[24:27], v[228:235], 0, v215, v215 op_sel_hi:[0,0,0] cbsz:4
	v_mfma_scale_f32_16x16x128_f8f6f4 v[156:159], v[28:31], v[228:235], 0, v215, v215 op_sel_hi:[0,0,0] cbsz:4
	s_lshl_b32 s78, s33, 8
	v_add_u32_e32 v248, s78, v240
	ds_read_b128 v[236:239], v248 offset:0
	s_waitcnt lgkmcnt(0)
	v_mad_u32_u16 v208, v236, s5, v241 op_sel:[0,0,0,0]
	global_load_dwordx4 v[0:3], v208, s[64:65]
	v_mad_u32_u16 v209, v236, s5, v241 op_sel:[1,0,0,0]
	global_load_dwordx4 v[4:7], v209, s[64:65]
	v_mad_u32_u16 v208, v237, s5, v241 op_sel:[0,0,0,0]
	global_load_dwordx4 v[8:11], v208, s[64:65]
	v_mad_u32_u16 v209, v237, s5, v241 op_sel:[1,0,0,0]
	global_load_dwordx4 v[12:15], v209, s[64:65]
	v_mad_u32_u16 v208, v238, s5, v241 op_sel:[0,0,0,0]
	global_load_dwordx4 v[16:19], v208, s[64:65]
	v_mad_u32_u16 v209, v238, s5, v241 op_sel:[1,0,0,0]
	global_load_dwordx4 v[20:23], v209, s[64:65]
	v_mad_u32_u16 v208, v239, s5, v241 op_sel:[0,0,0,0]
	global_load_dwordx4 v[24:27], v208, s[64:65]
	v_mad_u32_u16 v209, v239, s5, v241 op_sel:[1,0,0,0]
	global_load_dwordx4 v[28:31], v209, s[64:65]
	v_mov_b32_dpp v128, v128 quad_perm:[0,0,0,0] row_mask:0xf bank_mask:0xf
	v_mov_b32_dpp v132, v132 quad_perm:[0,0,0,0] row_mask:0xf bank_mask:0xf
	v_mov_b32_dpp v136, v136 quad_perm:[0,0,0,0] row_mask:0xf bank_mask:0xf
	v_mov_b32_dpp v140, v140 quad_perm:[0,0,0,0] row_mask:0xf bank_mask:0xf
	v_mov_b32_dpp v144, v144 quad_perm:[0,0,0,0] row_mask:0xf bank_mask:0xf
	v_mov_b32_dpp v148, v148 quad_perm:[0,0,0,0] row_mask:0xf bank_mask:0xf
	v_mov_b32_dpp v152, v152 quad_perm:[0,0,0,0] row_mask:0xf bank_mask:0xf
	v_mov_b32_dpp v156, v156 quad_perm:[0,0,0,0] row_mask:0xf bank_mask:0xf
	v_add_f32_dpp v128, v129, v128 quad_perm:[1,1,1,1] row_mask:0xf bank_mask:0xf
	v_add_f32_dpp v132, v133, v132 quad_perm:[1,1,1,1] row_mask:0xf bank_mask:0xf
	v_add_f32_dpp v136, v137, v136 quad_perm:[1,1,1,1] row_mask:0xf bank_mask:0xf
	v_add_f32_dpp v140, v141, v140 quad_perm:[1,1,1,1] row_mask:0xf bank_mask:0xf
	v_add_f32_dpp v144, v145, v144 quad_perm:[1,1,1,1] row_mask:0xf bank_mask:0xf
	v_add_f32_dpp v148, v149, v148 quad_perm:[1,1,1,1] row_mask:0xf bank_mask:0xf
	v_add_f32_dpp v152, v153, v152 quad_perm:[1,1,1,1] row_mask:0xf bank_mask:0xf
	v_add_f32_dpp v156, v157, v156 quad_perm:[1,1,1,1] row_mask:0xf bank_mask:0xf
	v_add_f32_dpp v128, v130, v128 quad_perm:[2,2,2,2] row_mask:0xf bank_mask:0xf
	v_add_f32_dpp v132, v134, v132 quad_perm:[2,2,2,2] row_mask:0xf bank_mask:0xf
	v_add_f32_dpp v136, v138, v136 quad_perm:[2,2,2,2] row_mask:0xf bank_mask:0xf
	v_add_f32_dpp v140, v142, v140 quad_perm:[2,2,2,2] row_mask:0xf bank_mask:0xf
	v_add_f32_dpp v144, v146, v144 quad_perm:[2,2,2,2] row_mask:0xf bank_mask:0xf
	v_add_f32_dpp v148, v150, v148 quad_perm:[2,2,2,2] row_mask:0xf bank_mask:0xf
	v_add_f32_dpp v152, v154, v152 quad_perm:[2,2,2,2] row_mask:0xf bank_mask:0xf
	v_add_f32_dpp v156, v158, v156 quad_perm:[2,2,2,2] row_mask:0xf bank_mask:0xf
	v_add_f32_dpp v128, v131, v128 quad_perm:[3,3,3,3] row_mask:0xf bank_mask:0xf
	v_add_f32_dpp v132, v135, v132 quad_perm:[3,3,3,3] row_mask:0xf bank_mask:0xf
	v_add_f32_dpp v136, v139, v136 quad_perm:[3,3,3,3] row_mask:0xf bank_mask:0xf
	v_add_f32_dpp v140, v143, v140 quad_perm:[3,3,3,3] row_mask:0xf bank_mask:0xf
	v_add_f32_dpp v144, v147, v144 quad_perm:[3,3,3,3] row_mask:0xf bank_mask:0xf
	v_add_f32_dpp v148, v151, v148 quad_perm:[3,3,3,3] row_mask:0xf bank_mask:0xf
	v_add_f32_dpp v152, v155, v152 quad_perm:[3,3,3,3] row_mask:0xf bank_mask:0xf
	v_add_f32_dpp v156, v159, v156 quad_perm:[3,3,3,3] row_mask:0xf bank_mask:0xf
	v_cndmask_b32_e32 v129, v128, v132, vcc
	v_cndmask_b32_e32 v137, v136, v140, vcc
	v_cndmask_b32_e32 v145, v144, v148, vcc
	v_cndmask_b32_e32 v153, v152, v156, vcc
	v_cndmask_b32_e64 v129, v129, v137, s[100:101]
	v_cndmask_b32_e64 v145, v145, v153, s[100:101]
	v_add_f32_e32 v246, v246, v129
	v_add_f32_e32 v247, v247, v145
	ds_write_b64 v210, v[246:247] offset:0
	ds_read_b64 v[246:247], v210 offset:512
	s_waitcnt vmcnt(26)
; #define LAS __attribute__((address_space(3)))
; #define XFENCE() asm volatile("" ::: "memory")
; __device__ __forceinline__ void expert_phase(const Frame& F, int l, int xcc, LAS unsigned char* wl, const LAS unsigned char* zb) {
;     ...
;             auto u_comp_h = [&](int hs, HRows& H) {
;                 const int k = (hs >> 1) & 7, mg = hs & 1;
;                 LAS f32x4* tp = (LAS f32x4*)(SA + k * 256 + (c & 1) * 16 + 4 * rq) + mg * 32;
;                 f32x4 acc[4];
; #pragma unroll
;                 for (int mm = 0; mm < 4; ++mm) acc[mm] = (f32x4){0.f, 0.f, 0.f, 0.f};
;                 if (c < 2) {
; #pragma unroll
;                     for (int mm = 0; mm < 4; ++mm) acc[mm] = tp[mm * 8];
;                 }
; #pragma unroll
;                 for (int mm = 0; mm < 4; ++mm) {
;                     const i32x8 a0 = {(int)H.r[2 * mm].x, (int)H.r[2 * mm].y, (int)H.r[2 * mm].z, (int)H.r[2 * mm].w, 0, 0, 0, 0};
;                     const i32x8 a1 = {(int)H.r[2 * mm + 1].x, (int)H.r[2 * mm + 1].y, (int)H.r[2 * mm + 1].z, (int)H.r[2 * mm + 1].w, 0, 0, 0, 0};
;                     acc[mm] = __builtin_amdgcn_mfma_scale_f32_16x16x128_f8f6f4(a0, B0, acc[mm], 4, 0, 0, 0x7F7F7F7F, 0, 0x7F7F7F7F);
;                     acc[mm] = __builtin_amdgcn_mfma_scale_f32_16x16x128_f8f6f4(a1, B1, acc[mm], 4, 0, 0, 0x7F7F7F7F, 0, 0x7F7F7F7F);
;                 }
;                 if (c < 2) {
; #pragma unroll
;                     for (int mm = 0; mm < 4; ++mm) tp[mm * 8] = acc[mm];
;                 }
;             };
;     ...
;                 u_rows_h(h4, H0); xe = u_x(i + 2 < 64 ? i + 2 : 63);
;                 XFENCE();
;                 u_comp_h(hs + 1, H1);
;                 XFENCE();
;                 u_rows_h(h5, H1);
;                 XFENCE();
;                 u_bbuild(i + 1, xo); u_comp_h(hs + 2, H2);
	v_mfma_scale_f32_16x16x128_f8f6f4 v[128:131], v[32:35], v[228:235], 0, v215, v215 op_sel_hi:[0,0,0] cbsz:4
	v_mfma_scale_f32_16x16x128_f8f6f4 v[132:135], v[36:39], v[228:235], 0, v215, v215 op_sel_hi:[0,0,0] cbsz:4
	v_mfma_scale_f32_16x16x128_f8f6f4 v[136:139], v[40:43], v[228:235], 0, v215, v215 op_sel_hi:[0,0,0] cbsz:4
	v_mfma_scale_f32_16x16x128_f8f6f4 v[140:143], v[44:47], v[228:235], 0, v215, v215 op_sel_hi:[0,0,0] cbsz:4
	v_mfma_scale_f32_16x16x128_f8f6f4 v[144:147], v[48:51], v[228:235], 0, v215, v215 op_sel_hi:[0,0,0] cbsz:4
	v_mfma_scale_f32_16x16x128_f8f6f4 v[148:151], v[52:55], v[228:235], 0, v215, v215 op_sel_hi:[0,0,0] cbsz:4
	v_mfma_scale_f32_16x16x128_f8f6f4 v[152:155], v[56:59], v[228:235], 0, v215, v215 op_sel_hi:[0,0,0] cbsz:4
	v_mfma_scale_f32_16x16x128_f8f6f4 v[156:159], v[60:63], v[228:235], 0, v215, v215 op_sel_hi:[0,0,0] cbsz:4
	s_lshl_b32 s78, s33, 8
	v_add_u32_e32 v248, s78, v240
	ds_read_b128 v[236:239], v248 offset:16
	s_waitcnt lgkmcnt(0)
	v_mad_u32_u16 v208, v236, s5, v241 op_sel:[0,0,0,0]
	global_load_dwordx4 v[32:35], v208, s[64:65]
	v_mad_u32_u16 v209, v236, s5, v241 op_sel:[1,0,0,0]
	global_load_dwordx4 v[36:39], v209, s[64:65]
	v_mad_u32_u16 v208, v237, s5, v241 op_sel:[0,0,0,0]
	global_load_dwordx4 v[40:43], v208, s[64:65]
	v_mad_u32_u16 v209, v237, s5, v241 op_sel:[1,0,0,0]
	global_load_dwordx4 v[44:47], v209, s[64:65]
	v_mad_u32_u16 v208, v238, s5, v241 op_sel:[0,0,0,0]
	global_load_dwordx4 v[48:51], v208, s[64:65]
	v_mad_u32_u16 v209, v238, s5, v241 op_sel:[1,0,0,0]
	global_load_dwordx4 v[52:55], v209, s[64:65]
	v_mad_u32_u16 v208, v239, s5, v241 op_sel:[0,0,0,0]
	global_load_dwordx4 v[56:59], v208, s[64:65]
	v_mad_u32_u16 v209, v239, s5, v241 op_sel:[1,0,0,0]
	global_load_dwordx4 v[60:63], v209, s[64:65]
	v_mov_b32_dpp v128, v128 quad_perm:[0,0,0,0] row_mask:0xf bank_mask:0xf
	v_mov_b32_dpp v132, v132 quad_perm:[0,0,0,0] row_mask:0xf bank_mask:0xf
	v_mov_b32_dpp v136, v136 quad_perm:[0,0,0,0] row_mask:0xf bank_mask:0xf
	v_mov_b32_dpp v140, v140 quad_perm:[0,0,0,0] row_mask:0xf bank_mask:0xf
	v_mov_b32_dpp v144, v144 quad_perm:[0,0,0,0] row_mask:0xf bank_mask:0xf
	v_mov_b32_dpp v148, v148 quad_perm:[0,0,0,0] row_mask:0xf bank_mask:0xf
	v_mov_b32_dpp v152, v152 quad_perm:[0,0,0,0] row_mask:0xf bank_mask:0xf
	v_mov_b32_dpp v156, v156 quad_perm:[0,0,0,0] row_mask:0xf bank_mask:0xf
	v_add_f32_dpp v128, v129, v128 quad_perm:[1,1,1,1] row_mask:0xf bank_mask:0xf
	v_add_f32_dpp v132, v133, v132 quad_perm:[1,1,1,1] row_mask:0xf bank_mask:0xf
	v_add_f32_dpp v136, v137, v136 quad_perm:[1,1,1,1] row_mask:0xf bank_mask:0xf
	v_add_f32_dpp v140, v141, v140 quad_perm:[1,1,1,1] row_mask:0xf bank_mask:0xf
	v_add_f32_dpp v144, v145, v144 quad_perm:[1,1,1,1] row_mask:0xf bank_mask:0xf
	v_add_f32_dpp v148, v149, v148 quad_perm:[1,1,1,1] row_mask:0xf bank_mask:0xf
	v_add_f32_dpp v152, v153, v152 quad_perm:[1,1,1,1] row_mask:0xf bank_mask:0xf
	v_add_f32_dpp v156, v157, v156 quad_perm:[1,1,1,1] row_mask:0xf bank_mask:0xf
	v_add_f32_dpp v128, v130, v128 quad_perm:[2,2,2,2] row_mask:0xf bank_mask:0xf
	v_add_f32_dpp v132, v134, v132 quad_perm:[2,2,2,2] row_mask:0xf bank_mask:0xf
	v_add_f32_dpp v136, v138, v136 quad_perm:[2,2,2,2] row_mask:0xf bank_mask:0xf
	v_add_f32_dpp v140, v142, v140 quad_perm:[2,2,2,2] row_mask:0xf bank_mask:0xf
	v_add_f32_dpp v144, v146, v144 quad_perm:[2,2,2,2] row_mask:0xf bank_mask:0xf
	v_add_f32_dpp v148, v150, v148 quad_perm:[2,2,2,2] row_mask:0xf bank_mask:0xf
	v_add_f32_dpp v152, v154, v152 quad_perm:[2,2,2,2] row_mask:0xf bank_mask:0xf
	v_add_f32_dpp v156, v158, v156 quad_perm:[2,2,2,2] row_mask:0xf bank_mask:0xf
	v_add_f32_dpp v128, v131, v128 quad_perm:[3,3,3,3] row_mask:0xf bank_mask:0xf
	v_add_f32_dpp v132, v135, v132 quad_perm:[3,3,3,3] row_mask:0xf bank_mask:0xf
	v_add_f32_dpp v136, v139, v136 quad_perm:[3,3,3,3] row_mask:0xf bank_mask:0xf
	v_add_f32_dpp v140, v143, v140 quad_perm:[3,3,3,3] row_mask:0xf bank_mask:0xf
	v_add_f32_dpp v144, v147, v144 quad_perm:[3,3,3,3] row_mask:0xf bank_mask:0xf
	v_add_f32_dpp v148, v151, v148 quad_perm:[3,3,3,3] row_mask:0xf bank_mask:0xf
	v_add_f32_dpp v152, v155, v152 quad_perm:[3,3,3,3] row_mask:0xf bank_mask:0xf
	v_add_f32_dpp v156, v159, v156 quad_perm:[3,3,3,3] row_mask:0xf bank_mask:0xf
	v_cndmask_b32_e32 v129, v128, v132, vcc
	v_cndmask_b32_e32 v137, v136, v140, vcc
	v_cndmask_b32_e32 v145, v144, v148, vcc
	v_cndmask_b32_e32 v153, v152, v156, vcc
	v_cndmask_b32_e64 v129, v129, v137, s[100:101]
	v_cndmask_b32_e64 v145, v145, v153, s[100:101]
	v_add_f32_e32 v246, v246, v129
	v_add_f32_e32 v247, v247, v145
	ds_write_b64 v210, v[246:247] offset:512
	s_add_i32 s77, s77, 1
	s_and_b32 s4, s77, 7
	s_lshl_b32 s78, s4, 2
	s_add_i32 s78, s78, s83
	v_mov_b32_e32 v152, s78
	s_lshr_b32 s78, s77, 3
	s_add_i32 s78, s78, s96
	s_and_b32 s78, s78, 7
	s_lshl_b32 s78, s78, 10
	v_add_u32_e32 v153, s78, v197
	ds_read_b32 v128, v152 offset:10240
	ds_read_b128 v[132:135], v153
	s_lshl_b32 s78, s4, 10
	s_add_i32 s78, s78, s83
	v_add_u32_e32 v210, s78, v184
	s_waitcnt vmcnt(33)
	v_lshlrev_b32_e32 v140, 16, v174
	v_and_b32_e32 v141, 0xffff0000, v174
	v_lshlrev_b32_e32 v142, 16, v175
	v_and_b32_e32 v143, 0xffff0000, v175
	v_mov_b32_e32 v144, 0
	v_mov_b32_e32 v145, 0
	s_waitcnt lgkmcnt(1)
	v_mul_f32_e32 v136, v128, v140
	v_mul_f32_e32 v137, v128, v141
	v_mul_f32_e32 v138, v128, v142
	v_mul_f32_e32 v139, v128, v143
	s_waitcnt lgkmcnt(0)
; #define LAS __attribute__((address_space(3)))
; __device__ __forceinline__ void expert_phase(const Frame& F, int l, int xcc, LAS unsigned char* wl, const LAS unsigned char* zb) {
;     ...
;             auto u_bbuild = [&](int i, const u32x2& xw) {
;                 const int k = i & 7;
;                 const f32x4 gg = *(const LAS f32x4*)(G2 + slice_of(i) * 256 + 4 * lane);
;                 const float rstd = RS[k];
;                 const float h0 = bf_lo(xw.x) * rstd * gg[0], h1 = bf_hi(xw.x) * rstd * gg[1], h2 = bf_lo(xw.y) * rstd * gg[2], h3 = bf_hi(xw.y) * rstd * gg[3];
;                 int w = __builtin_amdgcn_cvt_pk_fp8_f32(h0, h1, 0, false); w = __builtin_amdgcn_cvt_pk_fp8_f32(h2, h3, w, true);
;                 const f32x2 b0 = __builtin_amdgcn_cvt_pk_f32_fp8(w, false), b1 = __builtin_amdgcn_cvt_pk_f32_fp8(w, true);
;                 int v = __builtin_amdgcn_cvt_pk_fp8_f32(h0 - b0[0], h1 - b0[1], 0, false); v = __builtin_amdgcn_cvt_pk_fp8_f32(h2 - b1[0], h3 - b1[1], v, true);
;                 *(LAS int*)(bw) = w; *(LAS int*)(bw + 128) = v;
;                 LDS_WAIT(); XFENCE();
;                 const u32x4 b0l = *(const LAS u32x4*)(bbase), b0h = *(const LAS u32x4*)(bbase + 16), b1l = *(const LAS u32x4*)(bbase + 256), b1h = *(const LAS u32x4*)(bbase + 272);
;                 B0 = (i32x8){(int)b0l.x, (int)b0l.y, (int)b0l.z, (int)b0l.w, (int)b0h.x, (int)b0h.y, (int)b0h.z, (int)b0h.w};
;                 B1 = (i32x8){(int)b1l.x, (int)b1l.y, (int)b1l.z, (int)b1l.w, (int)b1h.x, (int)b1h.y, (int)b1h.z, (int)b1h.w};
;             };
;             auto u_comp_h = [&](int hs, HRows& H) {
;                 const int k = (hs >> 1) & 7, mg = hs & 1;
;                 LAS f32x4* tp = (LAS f32x4*)(SA + k * 256 + (c & 1) * 16 + 4 * rq) + mg * 32;
;                 f32x4 acc[4];
; #pragma unroll
;                 for (int mm = 0; mm < 4; ++mm) acc[mm] = (f32x4){0.f, 0.f, 0.f, 0.f};
;                 if (c < 2) {
; #pragma unroll
;                     for (int mm = 0; mm < 4; ++mm) acc[mm] = tp[mm * 8];
;                 }
; #pragma unroll
;                 for (int mm = 0; mm < 4; ++mm) {
;                     const i32x8 a0 = {(int)H.r[2 * mm].x, (int)H.r[2 * mm].y, (int)H.r[2 * mm].z, (int)H.r[2 * mm].w, 0, 0, 0, 0};
;                     const i32x8 a1 = {(int)H.r[2 * mm + 1].x, (int)H.r[2 * mm + 1].y, (int)H.r[2 * mm + 1].z, (int)H.r[2 * mm + 1].w, 0, 0, 0, 0};
	v_mul_f32_e32 v140, v132, v136
	v_mul_f32_e32 v141, v133, v137
	v_mul_f32_e32 v142, v134, v138
	v_mul_f32_e32 v143, v135, v139
	v_cvt_pk_fp8_f32 v144, v140, v141
	s_nop 0
	v_cvt_pk_fp8_f32 v144, v142, v143 op_sel:[0,0,1]
	s_nop 0
	v_cvt_pk_f32_fp8_e32 v[148:149], v144
	v_cvt_pk_f32_fp8_sdwa v[150:151], v144 src0_sel:WORD_1
	s_nop 0
	v_fma_f32 v140, v132, v136, -v148
	v_fma_f32 v141, v133, v137, -v149
	v_fma_f32 v142, v134, v138, -v150
	v_fma_f32 v143, v135, v139, -v151
	v_cvt_pk_fp8_f32 v145, v140, v141
	s_nop 0
	v_cvt_pk_fp8_f32 v145, v142, v143 op_sel:[0,0,1]
	v_add_u32_e32 v154, 0x2800, v207
	s_nop 0
	ds_write2_b32 v154, v144, v145 offset0:16 offset1:48
	s_waitcnt lgkmcnt(0)
	ds_read_b128 v[228:231], v242
	ds_read_b128 v[232:235], v249
	s_add_i32 s33, s77, 2
	s_min_i32 s33, s33, 63
	s_lshr_b32 s58, s33, 3
	s_add_i32 s58, s58, s96
	s_and_b32 s58, s58, 7
	s_and_b32 s33, s33, 7
	s_lshl_b32 s78, s58, 21
	s_add_u32 s64, s53, s78
	s_addc_u32 s65, s56, 0
	s_mul_i32 s78, s33, s82
	s_add_i32 s78, s78, s26
	s_cmpk_lt_i32 s78, 0x4000
	s_cselect_b32 s78, s78, s26
	s_ashr_i32 s55, s78, 31
	s_mov_b32 s54, s78
	s_lshl_b64 s[54:55], s[54:55], 12
	s_add_u32 s54, s90, s54
	s_addc_u32 s55, s91, s55
	s_lshl_b32 s78, s58, 9
	s_add_u32 s54, s54, s78
	s_addc_u32 s55, s55, 0
	v_lshl_add_u64 v[208:209], s[54:55], 0, v[184:185]
	global_load_dwordx2 v[174:175], v[208:209], off
	ds_read_b64 v[246:247], v210 offset:0
	s_waitcnt vmcnt(26) lgkmcnt(1)
	v_mfma_scale_f32_16x16x128_f8f6f4 v[128:131], v[64:67], v[228:235], 0, v215, v215 op_sel_hi:[0,0,0] cbsz:4
	v_mfma_scale_f32_16x16x128_f8f6f4 v[132:135], v[68:71], v[228:235], 0, v215, v215 op_sel_hi:[0,0,0] cbsz:4
	v_mfma_scale_f32_16x16x128_f8f6f4 v[136:139], v[72:75], v[228:235], 0, v215, v215 op_sel_hi:[0,0,0] cbsz:4
	v_mfma_scale_f32_16x16x128_f8f6f4 v[140:143], v[76:79], v[228:235], 0, v215, v215 op_sel_hi:[0,0,0] cbsz:4
	v_mfma_scale_f32_16x16x128_f8f6f4 v[144:147], v[80:83], v[228:235], 0, v215, v215 op_sel_hi:[0,0,0] cbsz:4
	v_mfma_scale_f32_16x16x128_f8f6f4 v[148:151], v[84:87], v[228:235], 0, v215, v215 op_sel_hi:[0,0,0] cbsz:4
	v_mfma_scale_f32_16x16x128_f8f6f4 v[152:155], v[88:91], v[228:235], 0, v215, v215 op_sel_hi:[0,0,0] cbsz:4
	v_mfma_scale_f32_16x16x128_f8f6f4 v[156:159], v[92:95], v[228:235], 0, v215, v215 op_sel_hi:[0,0,0] cbsz:4
	s_lshl_b32 s78, s33, 8
	v_add_u32_e32 v248, s78, v240
	ds_read_b128 v[236:239], v248 offset:0
	s_waitcnt lgkmcnt(0)
	v_mad_u32_u16 v208, v236, s5, v241 op_sel:[0,0,0,0]
	global_load_dwordx4 v[64:67], v208, s[64:65]
	v_mad_u32_u16 v209, v236, s5, v241 op_sel:[1,0,0,0]
	global_load_dwordx4 v[68:71], v209, s[64:65]
	v_mad_u32_u16 v208, v237, s5, v241 op_sel:[0,0,0,0]
	global_load_dwordx4 v[72:75], v208, s[64:65]
	v_mad_u32_u16 v209, v237, s5, v241 op_sel:[1,0,0,0]
	global_load_dwordx4 v[76:79], v209, s[64:65]
	v_mad_u32_u16 v208, v238, s5, v241 op_sel:[0,0,0,0]
	global_load_dwordx4 v[80:83], v208, s[64:65]
	v_mad_u32_u16 v209, v238, s5, v241 op_sel:[1,0,0,0]
	global_load_dwordx4 v[84:87], v209, s[64:65]
	v_mad_u32_u16 v208, v239, s5, v241 op_sel:[0,0,0,0]
	global_load_dwordx4 v[88:91], v208, s[64:65]
	v_mad_u32_u16 v209, v239, s5, v241 op_sel:[1,0,0,0]
	global_load_dwordx4 v[92:95], v209, s[64:65]
	v_mov_b32_dpp v128, v128 quad_perm:[0,0,0,0] row_mask:0xf bank_mask:0xf
	v_mov_b32_dpp v132, v132 quad_perm:[0,0,0,0] row_mask:0xf bank_mask:0xf
	v_mov_b32_dpp v136, v136 quad_perm:[0,0,0,0] row_mask:0xf bank_mask:0xf
	v_mov_b32_dpp v140, v140 quad_perm:[0,0,0,0] row_mask:0xf bank_mask:0xf
	v_mov_b32_dpp v144, v144 quad_perm:[0,0,0,0] row_mask:0xf bank_mask:0xf
	v_mov_b32_dpp v148, v148 quad_perm:[0,0,0,0] row_mask:0xf bank_mask:0xf
	v_mov_b32_dpp v152, v152 quad_perm:[0,0,0,0] row_mask:0xf bank_mask:0xf
	v_mov_b32_dpp v156, v156 quad_perm:[0,0,0,0] row_mask:0xf bank_mask:0xf
	v_add_f32_dpp v128, v129, v128 quad_perm:[1,1,1,1] row_mask:0xf bank_mask:0xf
	v_add_f32_dpp v132, v133, v132 quad_perm:[1,1,1,1] row_mask:0xf bank_mask:0xf
	v_add_f32_dpp v136, v137, v136 quad_perm:[1,1,1,1] row_mask:0xf bank_mask:0xf
	v_add_f32_dpp v140, v141, v140 quad_perm:[1,1,1,1] row_mask:0xf bank_mask:0xf
	v_add_f32_dpp v144, v145, v144 quad_perm:[1,1,1,1] row_mask:0xf bank_mask:0xf
	v_add_f32_dpp v148, v149, v148 quad_perm:[1,1,1,1] row_mask:0xf bank_mask:0xf
	v_add_f32_dpp v152, v153, v152 quad_perm:[1,1,1,1] row_mask:0xf bank_mask:0xf
	v_add_f32_dpp v156, v157, v156 quad_perm:[1,1,1,1] row_mask:0xf bank_mask:0xf
	v_add_f32_dpp v128, v130, v128 quad_perm:[2,2,2,2] row_mask:0xf bank_mask:0xf
	v_add_f32_dpp v132, v134, v132 quad_perm:[2,2,2,2] row_mask:0xf bank_mask:0xf
	v_add_f32_dpp v136, v138, v136 quad_perm:[2,2,2,2] row_mask:0xf bank_mask:0xf
	v_add_f32_dpp v140, v142, v140 quad_perm:[2,2,2,2] row_mask:0xf bank_mask:0xf
	v_add_f32_dpp v144, v146, v144 quad_perm:[2,2,2,2] row_mask:0xf bank_mask:0xf
	v_add_f32_dpp v148, v150, v148 quad_perm:[2,2,2,2] row_mask:0xf bank_mask:0xf
	v_add_f32_dpp v152, v154, v152 quad_perm:[2,2,2,2] row_mask:0xf bank_mask:0xf
	v_add_f32_dpp v156, v158, v156 quad_perm:[2,2,2,2] row_mask:0xf bank_mask:0xf
	v_add_f32_dpp v128, v131, v128 quad_perm:[3,3,3,3] row_mask:0xf bank_mask:0xf
	v_add_f32_dpp v132, v135, v132 quad_perm:[3,3,3,3] row_mask:0xf bank_mask:0xf
	v_add_f32_dpp v136, v139, v136 quad_perm:[3,3,3,3] row_mask:0xf bank_mask:0xf
	v_add_f32_dpp v140, v143, v140 quad_perm:[3,3,3,3] row_mask:0xf bank_mask:0xf
	v_add_f32_dpp v144, v147, v144 quad_perm:[3,3,3,3] row_mask:0xf bank_mask:0xf
	v_add_f32_dpp v148, v151, v148 quad_perm:[3,3,3,3] row_mask:0xf bank_mask:0xf
	v_add_f32_dpp v152, v155, v152 quad_perm:[3,3,3,3] row_mask:0xf bank_mask:0xf
	v_add_f32_dpp v156, v159, v156 quad_perm:[3,3,3,3] row_mask:0xf bank_mask:0xf
	v_cndmask_b32_e32 v129, v128, v132, vcc
	v_cndmask_b32_e32 v137, v136, v140, vcc
	v_cndmask_b32_e32 v145, v144, v148, vcc
	v_cndmask_b32_e32 v153, v152, v156, vcc
	v_cndmask_b32_e64 v129, v129, v137, s[100:101]
	v_cndmask_b32_e64 v145, v145, v153, s[100:101]
	v_add_f32_e32 v246, v246, v129
	v_add_f32_e32 v247, v247, v145
	ds_write_b64 v210, v[246:247] offset:0
	ds_read_b64 v[246:247], v210 offset:512
	s_waitcnt vmcnt(26)
; #define GAS __attribute__((address_space(1)))
; __device__ __forceinline__ void expert_phase(const Frame& F, int l, int xcc, LAS unsigned char* wl, const LAS unsigned char* zb) {
;     ...
;             auto u_comp_h = [&](int hs, HRows& H) {
;                 const int k = (hs >> 1) & 7, mg = hs & 1;
;                 LAS f32x4* tp = (LAS f32x4*)(SA + k * 256 + (c & 1) * 16 + 4 * rq) + mg * 32;
;                 f32x4 acc[4];
; #pragma unroll
;                 for (int mm = 0; mm < 4; ++mm) acc[mm] = (f32x4){0.f, 0.f, 0.f, 0.f};
;                 if (c < 2) {
; #pragma unroll
;                     for (int mm = 0; mm < 4; ++mm) acc[mm] = tp[mm * 8];
;                 }
; #pragma unroll
;                 for (int mm = 0; mm < 4; ++mm) {
;                     const i32x8 a0 = {(int)H.r[2 * mm].x, (int)H.r[2 * mm].y, (int)H.r[2 * mm].z, (int)H.r[2 * mm].w, 0, 0, 0, 0};
;                     const i32x8 a1 = {(int)H.r[2 * mm + 1].x, (int)H.r[2 * mm + 1].y, (int)H.r[2 * mm + 1].z, (int)H.r[2 * mm + 1].w, 0, 0, 0, 0};
;                     acc[mm] = __builtin_amdgcn_mfma_scale_f32_16x16x128_f8f6f4(a0, B0, acc[mm], 4, 0, 0, 0x7F7F7F7F, 0, 0x7F7F7F7F);
;                     acc[mm] = __builtin_amdgcn_mfma_scale_f32_16x16x128_f8f6f4(a1, B1, acc[mm], 4, 0, 0, 0x7F7F7F7F, 0, 0x7F7F7F7F);
;                 }
;                 if (c < 2) {
; #pragma unroll
;                     for (int mm = 0; mm < 4; ++mm) tp[mm * 8] = acc[mm];
;                 }
;             };
;     ...
;                 u_rows_h(h6, H2); xo = u_x(i + 3 < 64 ? i + 3 : 63);
;                 XFENCE();
;                 u_comp_h(hs + 3, H3);
;                 XFENCE();
;             }
;         }
;         LDS_WAIT(); XFENCE();
;         {
;             unsigned suvq[8][2]; float gtq[8][2];
; #pragma unroll
;             for (int k = 0; k < 8; ++k)
; #pragma unroll
;                 for (int hf = 0; hf < 2; ++hf) { const unsigned e = *(const LAS unsigned short*)(IDL + k * 256 + (hf * 64 + lane) * 2);
;                     suvq[k][hf] = *(const GAS unsigned*)(SUV + e); gtq[k][hf] = *(const GAS float*)(GATE + (size_t)tok(k) * 128 + hf * 64 + lane); }
; #pragma unroll
;             for (int k = 0; k < 8; ++k) {
;                 float wq[2];
; #pragma unroll
;                 for (int hf = 0; hf < 2; ++hf) {
;                     const unsigned suv = suvq[k][hf];
;                     const int kk = hf * 64 + lane;
	v_mfma_scale_f32_16x16x128_f8f6f4 v[128:131], v[96:99], v[228:235], 0, v215, v215 op_sel_hi:[0,0,0] cbsz:4
	v_mfma_scale_f32_16x16x128_f8f6f4 v[132:135], v[100:103], v[228:235], 0, v215, v215 op_sel_hi:[0,0,0] cbsz:4
	v_mfma_scale_f32_16x16x128_f8f6f4 v[136:139], v[104:107], v[228:235], 0, v215, v215 op_sel_hi:[0,0,0] cbsz:4
	v_mfma_scale_f32_16x16x128_f8f6f4 v[140:143], v[108:111], v[228:235], 0, v215, v215 op_sel_hi:[0,0,0] cbsz:4
	v_mfma_scale_f32_16x16x128_f8f6f4 v[144:147], v[112:115], v[228:235], 0, v215, v215 op_sel_hi:[0,0,0] cbsz:4
	v_mfma_scale_f32_16x16x128_f8f6f4 v[148:151], v[116:119], v[228:235], 0, v215, v215 op_sel_hi:[0,0,0] cbsz:4
	v_mfma_scale_f32_16x16x128_f8f6f4 v[152:155], v[120:123], v[228:235], 0, v215, v215 op_sel_hi:[0,0,0] cbsz:4
	v_mfma_scale_f32_16x16x128_f8f6f4 v[156:159], v[124:127], v[228:235], 0, v215, v215 op_sel_hi:[0,0,0] cbsz:4
	s_lshl_b32 s78, s33, 8
	v_add_u32_e32 v248, s78, v240
	ds_read_b128 v[236:239], v248 offset:16
	s_waitcnt lgkmcnt(0)
	v_mad_u32_u16 v208, v236, s5, v241 op_sel:[0,0,0,0]
	global_load_dwordx4 v[96:99], v208, s[64:65]
	v_mad_u32_u16 v209, v236, s5, v241 op_sel:[1,0,0,0]
	global_load_dwordx4 v[100:103], v209, s[64:65]
	v_mad_u32_u16 v208, v237, s5, v241 op_sel:[0,0,0,0]
	global_load_dwordx4 v[104:107], v208, s[64:65]
	v_mad_u32_u16 v209, v237, s5, v241 op_sel:[1,0,0,0]
	global_load_dwordx4 v[108:111], v209, s[64:65]
	v_mad_u32_u16 v208, v238, s5, v241 op_sel:[0,0,0,0]
	global_load_dwordx4 v[112:115], v208, s[64:65]
	v_mad_u32_u16 v209, v238, s5, v241 op_sel:[1,0,0,0]
	global_load_dwordx4 v[116:119], v209, s[64:65]
	v_mad_u32_u16 v208, v239, s5, v241 op_sel:[0,0,0,0]
	global_load_dwordx4 v[120:123], v208, s[64:65]
	v_mad_u32_u16 v209, v239, s5, v241 op_sel:[1,0,0,0]
	global_load_dwordx4 v[124:127], v209, s[64:65]
	v_mov_b32_dpp v128, v128 quad_perm:[0,0,0,0] row_mask:0xf bank_mask:0xf
	v_mov_b32_dpp v132, v132 quad_perm:[0,0,0,0] row_mask:0xf bank_mask:0xf
	v_mov_b32_dpp v136, v136 quad_perm:[0,0,0,0] row_mask:0xf bank_mask:0xf
	v_mov_b32_dpp v140, v140 quad_perm:[0,0,0,0] row_mask:0xf bank_mask:0xf
	v_mov_b32_dpp v144, v144 quad_perm:[0,0,0,0] row_mask:0xf bank_mask:0xf
	v_mov_b32_dpp v148, v148 quad_perm:[0,0,0,0] row_mask:0xf bank_mask:0xf
	v_mov_b32_dpp v152, v152 quad_perm:[0,0,0,0] row_mask:0xf bank_mask:0xf
	v_mov_b32_dpp v156, v156 quad_perm:[0,0,0,0] row_mask:0xf bank_mask:0xf
	v_add_f32_dpp v128, v129, v128 quad_perm:[1,1,1,1] row_mask:0xf bank_mask:0xf
	v_add_f32_dpp v132, v133, v132 quad_perm:[1,1,1,1] row_mask:0xf bank_mask:0xf
	v_add_f32_dpp v136, v137, v136 quad_perm:[1,1,1,1] row_mask:0xf bank_mask:0xf
	v_add_f32_dpp v140, v141, v140 quad_perm:[1,1,1,1] row_mask:0xf bank_mask:0xf
	v_add_f32_dpp v144, v145, v144 quad_perm:[1,1,1,1] row_mask:0xf bank_mask:0xf
	v_add_f32_dpp v148, v149, v148 quad_perm:[1,1,1,1] row_mask:0xf bank_mask:0xf
	v_add_f32_dpp v152, v153, v152 quad_perm:[1,1,1,1] row_mask:0xf bank_mask:0xf
	v_add_f32_dpp v156, v157, v156 quad_perm:[1,1,1,1] row_mask:0xf bank_mask:0xf
	v_add_f32_dpp v128, v130, v128 quad_perm:[2,2,2,2] row_mask:0xf bank_mask:0xf
	v_add_f32_dpp v132, v134, v132 quad_perm:[2,2,2,2] row_mask:0xf bank_mask:0xf
	v_add_f32_dpp v136, v138, v136 quad_perm:[2,2,2,2] row_mask:0xf bank_mask:0xf
	v_add_f32_dpp v140, v142, v140 quad_perm:[2,2,2,2] row_mask:0xf bank_mask:0xf
	v_add_f32_dpp v144, v146, v144 quad_perm:[2,2,2,2] row_mask:0xf bank_mask:0xf
	v_add_f32_dpp v148, v150, v148 quad_perm:[2,2,2,2] row_mask:0xf bank_mask:0xf
	v_add_f32_dpp v152, v154, v152 quad_perm:[2,2,2,2] row_mask:0xf bank_mask:0xf
	v_add_f32_dpp v156, v158, v156 quad_perm:[2,2,2,2] row_mask:0xf bank_mask:0xf
	v_add_f32_dpp v128, v131, v128 quad_perm:[3,3,3,3] row_mask:0xf bank_mask:0xf
	v_add_f32_dpp v132, v135, v132 quad_perm:[3,3,3,3] row_mask:0xf bank_mask:0xf
	v_add_f32_dpp v136, v139, v136 quad_perm:[3,3,3,3] row_mask:0xf bank_mask:0xf
	v_add_f32_dpp v140, v143, v140 quad_perm:[3,3,3,3] row_mask:0xf bank_mask:0xf
	v_add_f32_dpp v144, v147, v144 quad_perm:[3,3,3,3] row_mask:0xf bank_mask:0xf
	v_add_f32_dpp v148, v151, v148 quad_perm:[3,3,3,3] row_mask:0xf bank_mask:0xf
	v_add_f32_dpp v152, v155, v152 quad_perm:[3,3,3,3] row_mask:0xf bank_mask:0xf
	v_add_f32_dpp v156, v159, v156 quad_perm:[3,3,3,3] row_mask:0xf bank_mask:0xf
	v_cndmask_b32_e32 v129, v128, v132, vcc
	v_cndmask_b32_e32 v137, v136, v140, vcc
	v_cndmask_b32_e32 v145, v144, v148, vcc
	v_cndmask_b32_e32 v153, v152, v156, vcc
	v_cndmask_b32_e64 v129, v129, v137, s[100:101]
	v_cndmask_b32_e64 v145, v145, v153, s[100:101]
	v_add_f32_e32 v246, v246, v129
	v_add_f32_e32 v247, v247, v145
	ds_write_b64 v210, v[246:247] offset:512
	s_add_i32 s77, s77, 1
	s_cmp_lt_i32 s77, 64
	s_cbranch_scc1 .Lu_loop
	s_waitcnt vmcnt(0)
	v_add_u32_e32 v210, s83, v184
	ds_read_b64 v[0:1], v210 offset:0
	ds_read_b64 v[2:3], v210 offset:512
	ds_read_b64 v[4:5], v210 offset:1024
	ds_read_b64 v[6:7], v210 offset:1536
	ds_read_b64 v[8:9], v210 offset:2048
	ds_read_b64 v[10:11], v210 offset:2560
	ds_read_b64 v[12:13], v210 offset:3072
	ds_read_b64 v[14:15], v210 offset:3584
	ds_read_b64 v[16:17], v210 offset:4096
	ds_read_b64 v[18:19], v210 offset:4608
	ds_read_b64 v[20:21], v210 offset:5120
	ds_read_b64 v[22:23], v210 offset:5632
	ds_read_b64 v[24:25], v210 offset:6144
	ds_read_b64 v[26:27], v210 offset:6656
	ds_read_b64 v[28:29], v210 offset:7168
	ds_read_b64 v[30:31], v210 offset:7680
	s_waitcnt lgkmcnt(0)
	ds_write_b32 v243, v0 offset:0
	ds_write_b32 v243, v1 offset:512
	ds_write_b32 v243, v2 offset:4
	ds_write_b32 v243, v3 offset:516
	ds_write_b32 v243, v4 offset:1024
	ds_write_b32 v243, v5 offset:1536
	ds_write_b32 v243, v6 offset:1028
	ds_write_b32 v243, v7 offset:1540
	ds_write_b32 v243, v8 offset:2048
	ds_write_b32 v243, v9 offset:2560
	ds_write_b32 v243, v10 offset:2052
	ds_write_b32 v243, v11 offset:2564
	ds_write_b32 v243, v12 offset:3072
	ds_write_b32 v243, v13 offset:3584
	ds_write_b32 v243, v14 offset:3076
	ds_write_b32 v243, v15 offset:3588
	ds_write_b32 v243, v16 offset:4096
	ds_write_b32 v243, v17 offset:4608
	ds_write_b32 v243, v18 offset:4100
	ds_write_b32 v243, v19 offset:4612
	ds_write_b32 v243, v20 offset:5120
	ds_write_b32 v243, v21 offset:5632
	ds_write_b32 v243, v22 offset:5124
	ds_write_b32 v243, v23 offset:5636
	ds_write_b32 v243, v24 offset:6144
	ds_write_b32 v243, v25 offset:6656
	ds_write_b32 v243, v26 offset:6148
	ds_write_b32 v243, v27 offset:6660
	ds_write_b32 v243, v28 offset:7168
	ds_write_b32 v243, v29 offset:7680
	ds_write_b32 v243, v30 offset:7172
	ds_write_b32 v243, v31 offset:7684
	s_branch .LBB0_1159

; #define LAS __attribute__((address_space(3)))
; __device__ __forceinline__ void expert_phase(const Frame& F, int l, int xcc, LAS unsigned char* wl, const LAS unsigned char* zb) {
;     ...
;             auto v_rows = [&](int i, URows& R) {
;                 const unsigned char* Vsl = VBl + (size_t)slice_of(i) * XSL_BYTES;
;                 const u32x4 ia = *(const LAS u32x4*)(IDL + (i & 7) * 256 + rr * 32), ib = *(const LAS u32x4*)(IDL + (i & 7) * 256 + rr * 32 + 16);
; #pragma unroll
;                 for (int j = 0; j < 16; ++j) { const unsigned w = j < 8 ? ia[(j >> 1) & 3] : ib[(j >> 1) & 3]; const unsigned e = (j & 1) ? (w >> 16) : (w & 0xffffu);
;                     R.r[j] = ldo_u4(Vsl, e * 128u + 16u * pc); }
;             };
;             auto v_comp = [&](int i, const URows& R) {
;                 const int k = i & 7, t = tok(k), sl = slice_of(i);
;                 const unsigned col = 32u * pc + 4u * rr;
;                 u32x2 xw;
;                 typedef _Float16 hf2 __attribute__((ext_vector_type(2)));
;                 const LAS u32x4* wp = (const LAS u32x4*)(SA + k * 256 + 16 * rr);
;                 const u32x4 wall[4] = {wp[0], wp[1], wp[2], wp[3]};
;                 unsigned out[16];
; #pragma unroll
;                 for (int j = 0; j < 16; ++j) out[j] = 0u;
; #pragma unroll
;                 for (int j = 0; j < 16; ++j) {
;                     if (j == 8) xw = ldo_u2(X1 + (size_t)t * D + sl * 256, 2u * col);
;                     u32x4 rj = R.r[j];
;                     asm volatile("" : "+v"(rj.x), "+v"(rj.y), "+v"(rj.z), "+v"(rj.w) :: "memory");
;                     const unsigned wj = wall[j >> 2][j & 3]; const hf2 w2 = __builtin_bit_cast(hf2, wj);
; #pragma unroll
;                     for (int d = 0; d < 4; ++d) {
;                         const hf2 a = __builtin_amdgcn_cvt_scalef32_pk_f16_fp4(rj[d], 1.0f, 0), b = __builtin_amdgcn_cvt_scalef32_pk_f16_fp4(rj[d], 1.0f, 1),
;                                   cc = __builtin_amdgcn_cvt_scalef32_pk_f16_fp4(rj[d], 1.0f, 2), dd = __builtin_amdgcn_cvt_scalef32_pk_f16_fp4(rj[d], 1.0f, 3);
;                         out[4 * d] = __builtin_bit_cast(unsigned, __builtin_elementwise_fma(a, w2, __builtin_bit_cast(hf2, out[4 * d])));
;                         out[4 * d + 1] = __builtin_bit_cast(unsigned, __builtin_elementwise_fma(b, w2, __builtin_bit_cast(hf2, out[4 * d + 1])));
.LBB0_1239:
	s_or_b64 exec, exec, s[2:3]
	s_waitcnt vmcnt(0) lgkmcnt(0)
	v_and_b32_e32 v120, 7, v211
	v_lshrrev_b32_e32 v121, 3, v211
	v_and_b32_e32 v122, 15, v211
	v_lshrrev_b32_e32 v123, 4, v211
	s_lshr_b32 s2, s83, 10
	s_mul_i32 s2, s2, 79
	s_lshr_b32 s2, s2, 10
	s_mul_i32 s3, s2, 0x1200
	s_mov_b32 s8, 0x1c200
	s_mov_b32 s9, 0x1cc00
	s_cmp_lt_u32 s2, 3
	s_cselect_b32 s8, s8, s9
	s_mov_b32 s9, 0x1d400
	s_cmp_lt_u32 s2, 6
	s_cselect_b32 s8, s8, s9
	s_add_i32 s3, s3, s8
	v_lshlrev_b32_e32 v113, 4, v120
	v_mul_u32_u24_e32 v110, 0x240, v121
	v_add3_u32 v110, v110, v113, s3
	v_mul_u32_u24_e32 v111, 0x90, v122
	v_lshl_add_u32 v111, v123, 3, v111
	v_add_u32_e32 v111, s3, v111
	v_lshlrev_b32_e32 v112, 3, v121
	v_add_u32_e32 v112, s83, v112
	v_add_u32_e32 v112, 0x2a40, v112
	v_lshrrev_b32_e32 v124, 2, v122
	v_and_b32_e32 v125, 1, v123
	v_lshlrev_b32_e32 v114, 7, v124
	v_lshl_add_u32 v114, v125, 4, v114
	v_add_u32_e32 v114, s83, v114
	v_add_u32_e32 v114, 0x200, v114
	v_and_b32_e32 v126, 3, v211
	v_lshlrev_b32_e32 v115, 6, v126
	v_lshl_add_u32 v115, v123, 4, v115
	v_add_u32_e32 v115, s83, v115
	v_lshlrev_b32_e32 v116, 4, v122
	v_lshl_add_u32 v116, v123, 10, v116
	v_add_u32_e32 v116, s83, v116
	v_lshl_add_u32 v117, v211, 2, s83
	v_add_u32_e32 v117, 0x2000, v117
	v_lshl_add_u32 v118, v211, 2, s83
	v_add_u32_e32 v119, s83, v211
	v_add_u32_e32 v119, 0x200, v119
	s_mov_b32 s30, 0x1110111
	s_mov_b32 s31, 0x2220222
	s_mov_b32 s44, 0x4440444
	s_mov_b32 s45, 0x8880888
	s_mov_b32 s100, 0xf000f
	s_mov_b32 s101, 0xf000f
	s_mov_b32 s77, 0x7fff80
	s_mov_b32 s66, 0x07060302
	s_mov_b32 s68, 0x7fff
	ds_read2st64_b32 v[120:121], v118 offset0:0 offset1:1
	s_waitcnt lgkmcnt(0)
	v_cvt_f32_f16_e32 v122, v120
	v_cvt_f32_f16_e32 v123, v121
	v_cvt_pk_fp8_f32 v124, v122, v122
	v_cvt_pk_fp8_f32 v125, v123, v123
	s_nop 0
	ds_write_b8 v119, v124 offset:0
	ds_write_b8 v119, v125 offset:64
	v_cvt_f32_fp8_e32 v126, v124
	v_cvt_f32_fp8_e32 v127, v125
	s_nop 0
	v_sub_f32_e32 v128, v122, v126
	v_sub_f32_e32 v129, v123, v127
	v_cvt_pk_fp8_f32 v124, v128, v128
	v_cvt_pk_fp8_f32 v125, v129, v129
	s_nop 0
	ds_write_b8 v119, v124 offset:128
	ds_write_b8 v119, v125 offset:192
	v_cvt_f32_fp8_e32 v126, v124
	v_cvt_f32_fp8_e32 v127, v125
	s_nop 0
	v_sub_f32_e32 v128, v128, v126
	v_sub_f32_e32 v129, v129, v127
	v_cvt_pk_fp8_f32 v124, v128, v128
	v_cvt_pk_fp8_f32 v125, v129, v129
	s_nop 0
	ds_write_b8 v119, v124 offset:256
	ds_write_b8 v119, v125 offset:320
	ds_read2st64_b32 v[120:121], v118 offset0:4 offset1:5
	s_waitcnt lgkmcnt(0)
	v_cvt_f32_f16_e32 v122, v120
	v_cvt_f32_f16_e32 v123, v121
	v_cvt_pk_fp8_f32 v124, v122, v122
	v_cvt_pk_fp8_f32 v125, v123, v123
	s_nop 0
	ds_write_b8 v119, v124 offset:1024
	ds_write_b8 v119, v125 offset:1088
	v_cvt_f32_fp8_e32 v126, v124
	v_cvt_f32_fp8_e32 v127, v125
	s_nop 0
	v_sub_f32_e32 v128, v122, v126
	v_sub_f32_e32 v129, v123, v127
	v_cvt_pk_fp8_f32 v124, v128, v128
	v_cvt_pk_fp8_f32 v125, v129, v129
	s_nop 0
	ds_write_b8 v119, v124 offset:1152
	ds_write_b8 v119, v125 offset:1216
	v_cvt_f32_fp8_e32 v126, v124
	v_cvt_f32_fp8_e32 v127, v125
	s_nop 0
	v_sub_f32_e32 v128, v128, v126
	v_sub_f32_e32 v129, v129, v127
	v_cvt_pk_fp8_f32 v124, v128, v128
	v_cvt_pk_fp8_f32 v125, v129, v129
	s_nop 0
	ds_write_b8 v119, v124 offset:1280
	ds_write_b8 v119, v125 offset:1344
	ds_read2st64_b32 v[120:121], v118 offset0:8 offset1:9
	s_waitcnt lgkmcnt(0)
	v_cvt_f32_f16_e32 v122, v120
	v_cvt_f32_f16_e32 v123, v121
	v_cvt_pk_fp8_f32 v124, v122, v122
	v_cvt_pk_fp8_f32 v125, v123, v123
	s_nop 0
	ds_write_b8 v119, v124 offset:2048
	ds_write_b8 v119, v125 offset:2112
	v_cvt_f32_fp8_e32 v126, v124
	v_cvt_f32_fp8_e32 v127, v125
	s_nop 0
	v_sub_f32_e32 v128, v122, v126
	v_sub_f32_e32 v129, v123, v127
	v_cvt_pk_fp8_f32 v124, v128, v128
	v_cvt_pk_fp8_f32 v125, v129, v129
	s_nop 0
	ds_write_b8 v119, v124 offset:2176
	ds_write_b8 v119, v125 offset:2240
	v_cvt_f32_fp8_e32 v126, v124
	v_cvt_f32_fp8_e32 v127, v125
	s_nop 0
	v_sub_f32_e32 v128, v128, v126
	v_sub_f32_e32 v129, v129, v127
	v_cvt_pk_fp8_f32 v124, v128, v128
	v_cvt_pk_fp8_f32 v125, v129, v129
	s_nop 0
	ds_write_b8 v119, v124 offset:2304
	ds_write_b8 v119, v125 offset:2368
	ds_read2st64_b32 v[120:121], v118 offset0:12 offset1:13
	s_waitcnt lgkmcnt(0)
	v_cvt_f32_f16_e32 v122, v120
	v_cvt_f32_f16_e32 v123, v121
	v_cvt_pk_fp8_f32 v124, v122, v122
	v_cvt_pk_fp8_f32 v125, v123, v123
	s_nop 0
	ds_write_b8 v119, v124 offset:3072
	ds_write_b8 v119, v125 offset:3136
	v_cvt_f32_fp8_e32 v126, v124
	v_cvt_f32_fp8_e32 v127, v125
	s_nop 0
	v_sub_f32_e32 v128, v122, v126
	v_sub_f32_e32 v129, v123, v127
	v_cvt_pk_fp8_f32 v124, v128, v128
	v_cvt_pk_fp8_f32 v125, v129, v129
	s_nop 0
	ds_write_b8 v119, v124 offset:3200
	ds_write_b8 v119, v125 offset:3264
	v_cvt_f32_fp8_e32 v126, v124
	v_cvt_f32_fp8_e32 v127, v125
	s_nop 0
	v_sub_f32_e32 v128, v128, v126
	v_sub_f32_e32 v129, v129, v127
	v_cvt_pk_fp8_f32 v124, v128, v128
	v_cvt_pk_fp8_f32 v125, v129, v129
	s_nop 0
	ds_write_b8 v119, v124 offset:3328
	ds_write_b8 v119, v125 offset:3392
	ds_read2st64_b32 v[120:121], v118 offset0:16 offset1:17
	s_waitcnt lgkmcnt(0)
	v_cvt_f32_f16_e32 v122, v120
	v_cvt_f32_f16_e32 v123, v121
	v_cvt_pk_fp8_f32 v124, v122, v122
	v_cvt_pk_fp8_f32 v125, v123, v123
	s_nop 0
	ds_write_b8 v119, v124 offset:4096
	ds_write_b8 v119, v125 offset:4160
	v_cvt_f32_fp8_e32 v126, v124
	v_cvt_f32_fp8_e32 v127, v125
	s_nop 0
	v_sub_f32_e32 v128, v122, v126
	v_sub_f32_e32 v129, v123, v127
	v_cvt_pk_fp8_f32 v124, v128, v128
	v_cvt_pk_fp8_f32 v125, v129, v129
	s_nop 0
	ds_write_b8 v119, v124 offset:4224
	ds_write_b8 v119, v125 offset:4288
	v_cvt_f32_fp8_e32 v126, v124
	v_cvt_f32_fp8_e32 v127, v125
	s_nop 0
	v_sub_f32_e32 v128, v128, v126
	v_sub_f32_e32 v129, v129, v127
	v_cvt_pk_fp8_f32 v124, v128, v128
	v_cvt_pk_fp8_f32 v125, v129, v129
	s_nop 0
	ds_write_b8 v119, v124 offset:4352
	ds_write_b8 v119, v125 offset:4416
	ds_read2st64_b32 v[120:121], v118 offset0:20 offset1:21
	s_waitcnt lgkmcnt(0)
; #define LAS __attribute__((address_space(3)))
; #define XFENCE() asm volatile("" ::: "memory")
; __device__ __forceinline__ void expert_phase(const Frame& F, int l, int xcc, LAS unsigned char* wl, const LAS unsigned char* zb) {
;     ...
;             auto v_rows = [&](int i, URows& R) {
;                 const unsigned char* Vsl = VBl + (size_t)slice_of(i) * XSL_BYTES;
;                 const u32x4 ia = *(const LAS u32x4*)(IDL + (i & 7) * 256 + rr * 32), ib = *(const LAS u32x4*)(IDL + (i & 7) * 256 + rr * 32 + 16);
; #pragma unroll
;                 for (int j = 0; j < 16; ++j) { const unsigned w = j < 8 ? ia[(j >> 1) & 3] : ib[(j >> 1) & 3]; const unsigned e = (j & 1) ? (w >> 16) : (w & 0xffffu);
;                     R.r[j] = ldo_u4(Vsl, e * 128u + 16u * pc); }
;             };
;     ...
;             URows RA, RB;
;             v_rows(0, RA);
;             XFENCE();
; #pragma unroll 1
;             for (int i = 0; i < 64; i += 2) {
;                 const int i2 = i + 2 < 64 ? i + 2 : 63;
;                 v_rows(i + 1, RB);
;                 XFENCE();
	v_cvt_f32_f16_e32 v122, v120
	v_cvt_f32_f16_e32 v123, v121
	v_cvt_pk_fp8_f32 v124, v122, v122
	v_cvt_pk_fp8_f32 v125, v123, v123
	s_nop 0
	ds_write_b8 v119, v124 offset:5120
	ds_write_b8 v119, v125 offset:5184
	v_cvt_f32_fp8_e32 v126, v124
	v_cvt_f32_fp8_e32 v127, v125
	s_nop 0
	v_sub_f32_e32 v128, v122, v126
	v_sub_f32_e32 v129, v123, v127
	v_cvt_pk_fp8_f32 v124, v128, v128
	v_cvt_pk_fp8_f32 v125, v129, v129
	s_nop 0
	ds_write_b8 v119, v124 offset:5248
	ds_write_b8 v119, v125 offset:5312
	v_cvt_f32_fp8_e32 v126, v124
	v_cvt_f32_fp8_e32 v127, v125
	s_nop 0
	v_sub_f32_e32 v128, v128, v126
	v_sub_f32_e32 v129, v129, v127
	v_cvt_pk_fp8_f32 v124, v128, v128
	v_cvt_pk_fp8_f32 v125, v129, v129
	s_nop 0
	ds_write_b8 v119, v124 offset:5376
	ds_write_b8 v119, v125 offset:5440
	ds_read2st64_b32 v[120:121], v118 offset0:24 offset1:25
	s_waitcnt lgkmcnt(0)
	v_cvt_f32_f16_e32 v122, v120
	v_cvt_f32_f16_e32 v123, v121
	v_cvt_pk_fp8_f32 v124, v122, v122
	v_cvt_pk_fp8_f32 v125, v123, v123
	s_nop 0
	ds_write_b8 v119, v124 offset:6144
	ds_write_b8 v119, v125 offset:6208
	v_cvt_f32_fp8_e32 v126, v124
	v_cvt_f32_fp8_e32 v127, v125
	s_nop 0
	v_sub_f32_e32 v128, v122, v126
	v_sub_f32_e32 v129, v123, v127
	v_cvt_pk_fp8_f32 v124, v128, v128
	v_cvt_pk_fp8_f32 v125, v129, v129
	s_nop 0
	ds_write_b8 v119, v124 offset:6272
	ds_write_b8 v119, v125 offset:6336
	v_cvt_f32_fp8_e32 v126, v124
	v_cvt_f32_fp8_e32 v127, v125
	s_nop 0
	v_sub_f32_e32 v128, v128, v126
	v_sub_f32_e32 v129, v129, v127
	v_cvt_pk_fp8_f32 v124, v128, v128
	v_cvt_pk_fp8_f32 v125, v129, v129
	s_nop 0
	ds_write_b8 v119, v124 offset:6400
	ds_write_b8 v119, v125 offset:6464
	ds_read2st64_b32 v[120:121], v118 offset0:28 offset1:29
	s_waitcnt lgkmcnt(0)
	v_cvt_f32_f16_e32 v122, v120
	v_cvt_f32_f16_e32 v123, v121
	v_cvt_pk_fp8_f32 v124, v122, v122
	v_cvt_pk_fp8_f32 v125, v123, v123
	s_nop 0
	ds_write_b8 v119, v124 offset:7168
	ds_write_b8 v119, v125 offset:7232
	v_cvt_f32_fp8_e32 v126, v124
	v_cvt_f32_fp8_e32 v127, v125
	s_nop 0
	v_sub_f32_e32 v128, v122, v126
	v_sub_f32_e32 v129, v123, v127
	v_cvt_pk_fp8_f32 v124, v128, v128
	v_cvt_pk_fp8_f32 v125, v129, v129
	s_nop 0
	ds_write_b8 v119, v124 offset:7296
	ds_write_b8 v119, v125 offset:7360
	v_cvt_f32_fp8_e32 v126, v124
	v_cvt_f32_fp8_e32 v127, v125
	s_nop 0
	v_sub_f32_e32 v128, v128, v126
	v_sub_f32_e32 v129, v129, v127
	v_cvt_pk_fp8_f32 v124, v128, v128
	v_cvt_pk_fp8_f32 v125, v129, v129
	s_nop 0
	ds_write_b8 v119, v124 offset:7424
	ds_write_b8 v119, v125 offset:7488
	s_mov_b32 s67, 0
	s_and_b32 s33, s67, 7
	s_lshr_b32 s58, s67, 3
	s_add_i32 s58, s58, s96
	s_and_b32 s58, s58, 7
	s_mul_i32 s8, s33, s82
	s_add_i32 s8, s8, s26
	s_cmpk_lt_i32 s8, 0x4000
	s_cselect_b32 s8, s8, s26
	s_lshl_b32 s78, s58, 21
	s_add_u32 s64, s57, s78
	s_addc_u32 s65, s70, 0
	s_lshl_b32 s78, s33, 8
	v_add_u32_e32 v123, s78, v112
	ds_read_b64 v[108:109], v123 offset:0
	s_waitcnt lgkmcnt(0)
	v_lshlrev_b32_e32 v208, 7, v108
	v_and_or_b32 v208, v208, s77, v113
	global_load_dwordx4 v[0:3], v208, s[64:65]
	v_bfe_u32 v209, v108, 16, 16
	v_lshl_or_b32 v209, v209, 7, v113
	global_load_dwordx4 v[4:7], v209, s[64:65]
	v_lshlrev_b32_e32 v208, 7, v109
	v_and_or_b32 v208, v208, s77, v113
	global_load_dwordx4 v[8:11], v208, s[64:65]
	v_bfe_u32 v209, v109, 16, 16
	v_lshl_or_b32 v209, v209, 7, v113
	global_load_dwordx4 v[12:15], v209, s[64:65]
	s_lshl_b32 s78, s33, 8
	v_add_u32_e32 v123, s78, v112
	ds_read_b64 v[226:227], v123 offset:64
	s_waitcnt lgkmcnt(0)
	v_lshlrev_b32_e32 v208, 7, v226
	v_and_or_b32 v208, v208, s77, v113
	global_load_dwordx4 v[16:19], v208, s[64:65]
	v_bfe_u32 v209, v226, 16, 16
	v_lshl_or_b32 v209, v209, 7, v113
	global_load_dwordx4 v[20:23], v209, s[64:65]
	v_lshlrev_b32_e32 v208, 7, v227
	v_and_or_b32 v208, v208, s77, v113
	global_load_dwordx4 v[24:27], v208, s[64:65]
	v_bfe_u32 v209, v227, 16, 16
	v_lshl_or_b32 v209, v209, 7, v113
	global_load_dwordx4 v[28:31], v209, s[64:65]
	s_lshl_b32 s78, s33, 8
	v_add_u32_e32 v123, s78, v112
	ds_read_b64 v[108:109], v123 offset:128
	s_waitcnt lgkmcnt(0)
	v_lshlrev_b32_e32 v208, 7, v108
	v_and_or_b32 v208, v208, s77, v113
	global_load_dwordx4 v[32:35], v208, s[64:65]
	v_bfe_u32 v209, v108, 16, 16
	v_lshl_or_b32 v209, v209, 7, v113
	global_load_dwordx4 v[36:39], v209, s[64:65]
	v_lshlrev_b32_e32 v208, 7, v109
	v_and_or_b32 v208, v208, s77, v113
	global_load_dwordx4 v[40:43], v208, s[64:65]
	v_bfe_u32 v209, v109, 16, 16
	v_lshl_or_b32 v209, v209, 7, v113
	global_load_dwordx4 v[44:47], v209, s[64:65]
	s_lshl_b32 s78, s33, 8
	v_add_u32_e32 v123, s78, v112
	ds_read_b64 v[226:227], v123 offset:192
	s_waitcnt lgkmcnt(0)
	v_lshlrev_b32_e32 v208, 7, v226
	v_and_or_b32 v208, v208, s77, v113
	global_load_dwordx4 v[48:51], v208, s[64:65]
	v_bfe_u32 v209, v226, 16, 16
	v_lshl_or_b32 v209, v209, 7, v113
	global_load_dwordx4 v[52:55], v209, s[64:65]
	v_lshlrev_b32_e32 v208, 7, v227
	v_and_or_b32 v208, v208, s77, v113
	global_load_dwordx4 v[56:59], v208, s[64:65]
	v_bfe_u32 v209, v227, 16, 16
	v_lshl_or_b32 v209, v209, 7, v113
	global_load_dwordx4 v[60:63], v209, s[64:65]
	s_ashr_i32 s55, s8, 31
	s_mov_b32 s54, s8
	s_lshl_b64 s[54:55], s[54:55], 12
	s_add_u32 s54, s90, s54
	s_addc_u32 s55, s91, s55
	s_lshl_b32 s78, s58, 9
	s_add_u32 s54, s54, s78
	s_addc_u32 s55, s55, 0
	v_lshl_add_u64 v[208:209], s[54:55], 0, v[184:185]
	global_load_dwordx2 v[172:173], v[208:209], off
	s_mov_b32 s4, 1
	s_and_b32 s33, s4, 7
	s_lshr_b32 s58, s4, 3
	s_add_i32 s58, s58, s96
	s_and_b32 s58, s58, 7
	s_mul_i32 s9, s33, s82
	s_add_i32 s9, s9, s26
	s_cmpk_lt_i32 s9, 0x4000
	s_cselect_b32 s9, s9, s26
	s_mov_b32 s2, 0
	s_waitcnt vmcnt(12)
	ds_write_b128 v110, v[0:3] offset:0
	ds_write_b128 v110, v[4:7] offset:144
	ds_write_b128 v110, v[8:11] offset:288
	ds_write_b128 v110, v[12:15] offset:432
	s_lshl_b32 s78, s2, 10
	v_add_u32_e32 v120, s78, v114
	v_mov_b32_e32 v121, 0x1a000
	v_cndmask_b32_e64 v122, v121, v120, s[30:31]
	v_cndmask_b32_e64 v121, v121, v120, s[44:45]
	ds_read_b128 v[80:83], v122
	ds_read_b128 v[84:87], v121
	s_lshl_b32 s78, s33, 8
	v_add_u32_e32 v123, s78, v112
	ds_read_b64 v[108:109], v123 offset:0
	ds_read_b64_tr_b4 v[64:65], v111 offset:0
	ds_read_b64_tr_b4 v[66:67], v111 offset:2304
	ds_read_b64_tr_b4 v[68:69], v111 offset:32
	ds_read_b64_tr_b4 v[70:71], v111 offset:2336
	ds_read_b64_tr_b4 v[72:73], v111 offset:64
	ds_read_b64_tr_b4 v[74:75], v111 offset:2368
	ds_read_b64_tr_b4 v[76:77], v111 offset:96
	ds_read_b64_tr_b4 v[78:79], v111 offset:2400
; #define LAS __attribute__((address_space(3)))
; __device__ __forceinline__ void expert_phase(const Frame& F, int l, int xcc, LAS unsigned char* wl, const LAS unsigned char* zb) {
;     ...
;                 const u32x4 ia = *(const LAS u32x4*)(IDL + (i & 7) * 256 + rr * 32), ib = *(const LAS u32x4*)(IDL + (i & 7) * 256 + rr * 32 + 16);
; #pragma unroll
;                 for (int j = 0; j < 16; ++j) { const unsigned w = j < 8 ? ia[(j >> 1) & 3] : ib[(j >> 1) & 3]; const unsigned e = (j & 1) ? (w >> 16) : (w & 0xffffu);
;                     R.r[j] = ldo_u4(Vsl, e * 128u + 16u * pc); }
;             };
;             auto v_comp = [&](int i, const URows& R) {
;                 const int k = i & 7, t = tok(k), sl = slice_of(i);
;                 const unsigned col = 32u * pc + 4u * rr;
;                 u32x2 xw;
;                 typedef _Float16 hf2 __attribute__((ext_vector_type(2)));
;                 const LAS u32x4* wp = (const LAS u32x4*)(SA + k * 256 + 16 * rr);
;                 const u32x4 wall[4] = {wp[0], wp[1], wp[2], wp[3]};
;                 unsigned out[16];
; #pragma unroll
;                 for (int j = 0; j < 16; ++j) out[j] = 0u;
; #pragma unroll
;                 for (int j = 0; j < 16; ++j) {
;                     if (j == 8) xw = ldo_u2(X1 + (size_t)t * D + sl * 256, 2u * col);
;                     u32x4 rj = R.r[j];
;                     asm volatile("" : "+v"(rj.x), "+v"(rj.y), "+v"(rj.z), "+v"(rj.w) :: "memory");
;                     const unsigned wj = wall[j >> 2][j & 3]; const hf2 w2 = __builtin_bit_cast(hf2, wj);
; #pragma unroll
;                     for (int d = 0; d < 4; ++d) {
;                         const hf2 a = __builtin_amdgcn_cvt_scalef32_pk_f16_fp4(rj[d], 1.0f, 0), b = __builtin_amdgcn_cvt_scalef32_pk_f16_fp4(rj[d], 1.0f, 1),
;                                   cc = __builtin_amdgcn_cvt_scalef32_pk_f16_fp4(rj[d], 1.0f, 2), dd = __builtin_amdgcn_cvt_scalef32_pk_f16_fp4(rj[d], 1.0f, 3);
;                         out[4 * d] = __builtin_bit_cast(unsigned, __builtin_elementwise_fma(a, w2, __builtin_bit_cast(hf2, out[4 * d])));
;                         out[4 * d + 1] = __builtin_bit_cast(unsigned, __builtin_elementwise_fma(b, w2, __builtin_bit_cast(hf2, out[4 * d + 1])));
;                         out[4 * d + 2] = __builtin_bit_cast(unsigned, __builtin_elementwise_fma(cc, w2, __builtin_bit_cast(hf2, out[4 * d + 2])));
.Lv_loop:
	s_and_b32 s2, s67, 7
	s_lshr_b32 s3, s67, 3
	s_add_i32 s3, s3, s96
	s_and_b32 s3, s3, 7
	s_mul_i32 s8, s2, s82
	s_add_i32 s8, s8, s26
	s_cmpk_lt_i32 s8, 0x4000
	s_cselect_b32 s8, s8, s26
	s_add_i32 s4, s67, 1
	s_min_i32 s4, s4, 63
	s_and_b32 s33, s4, 7
	s_lshr_b32 s58, s4, 3
	s_add_i32 s58, s58, s96
	s_and_b32 s58, s58, 7
	s_mul_i32 s9, s33, s82
	s_add_i32 s9, s9, s26
	s_cmpk_lt_i32 s9, 0x4000
	s_cselect_b32 s9, s9, s26
	s_lshl_b32 s78, s58, 21
	s_add_u32 s64, s57, s78
	s_addc_u32 s65, s70, 0
	s_waitcnt lgkmcnt(0)
	s_waitcnt vmcnt(9)
	v_mfma_scale_f32_16x16x128_f8f6f4 v[88:91], v[64:67], v[80:87], 0, v215, v215 op_sel_hi:[0,0,0] cbsz:4
	ds_write_b128 v110, v[16:19] offset:0
	v_lshlrev_b32_e32 v208, 7, v108
	v_and_or_b32 v208, v208, s77, v113
	global_load_dwordx4 v[0:3], v208, s[64:65]
	v_mfma_scale_f32_16x16x128_f8f6f4 v[92:95], v[68:71], v[80:87], 0, v215, v215 op_sel_hi:[0,0,0] cbsz:4
	ds_write_b128 v110, v[20:23] offset:144
	v_bfe_u32 v209, v108, 16, 16
	v_lshl_or_b32 v209, v209, 7, v113
	global_load_dwordx4 v[4:7], v209, s[64:65]
	v_mfma_scale_f32_16x16x128_f8f6f4 v[96:99], v[72:75], v[80:87], 0, v215, v215 op_sel_hi:[0,0,0] cbsz:4
	ds_write_b128 v110, v[24:27] offset:288
	v_lshlrev_b32_e32 v208, 7, v109
	v_and_or_b32 v208, v208, s77, v113
	global_load_dwordx4 v[8:11], v208, s[64:65]
	v_mfma_scale_f32_16x16x128_f8f6f4 v[100:103], v[76:79], v[80:87], 0, v215, v215 op_sel_hi:[0,0,0] cbsz:4
	ds_write_b128 v110, v[28:31] offset:432
	v_bfe_u32 v209, v109, 16, 16
	v_lshl_or_b32 v209, v209, 7, v113
	global_load_dwordx4 v[12:15], v209, s[64:65]
	s_lshl_b32 s78, s2, 10
	s_add_i32 s78, s78, 32
	v_add_u32_e32 v120, s78, v114
	v_mov_b32_e32 v121, 0x1a000
	v_cndmask_b32_e64 v122, v121, v120, s[30:31]
	v_cndmask_b32_e64 v121, v121, v120, s[44:45]
	ds_read_b128 v[152:155], v122
	ds_read_b128 v[156:159], v121
	s_lshl_b32 s78, s33, 8
	v_add_u32_e32 v123, s78, v112
	ds_read_b64 v[226:227], v123 offset:64
	ds_read_b64_tr_b4 v[136:137], v111 offset:0
	ds_read_b64_tr_b4 v[138:139], v111 offset:2304
	ds_read_b64_tr_b4 v[140:141], v111 offset:32
	ds_read_b64_tr_b4 v[142:143], v111 offset:2336
	ds_read_b64_tr_b4 v[144:145], v111 offset:64
	ds_read_b64_tr_b4 v[146:147], v111 offset:2368
	ds_read_b64_tr_b4 v[148:149], v111 offset:96
	ds_read_b64_tr_b4 v[150:151], v111 offset:2400
	s_waitcnt lgkmcnt(0)
	s_waitcnt vmcnt(9)
	v_mfma_scale_f32_16x16x128_f8f6f4 v[88:91], v[136:139], v[152:159], v[88:91], v215, v215 op_sel_hi:[0,0,0] cbsz:4
	ds_write_b128 v110, v[32:35] offset:0
	v_lshlrev_b32_e32 v208, 7, v226
	v_and_or_b32 v208, v208, s77, v113
	global_load_dwordx4 v[16:19], v208, s[64:65]
	v_mfma_scale_f32_16x16x128_f8f6f4 v[92:95], v[140:143], v[152:159], v[92:95], v215, v215 op_sel_hi:[0,0,0] cbsz:4
	ds_write_b128 v110, v[36:39] offset:144
	v_bfe_u32 v209, v226, 16, 16
	v_lshl_or_b32 v209, v209, 7, v113
	global_load_dwordx4 v[20:23], v209, s[64:65]
	v_mfma_scale_f32_16x16x128_f8f6f4 v[96:99], v[144:147], v[152:159], v[96:99], v215, v215 op_sel_hi:[0,0,0] cbsz:4
	ds_write_b128 v110, v[40:43] offset:288
	v_lshlrev_b32_e32 v208, 7, v227
	v_and_or_b32 v208, v208, s77, v113
	global_load_dwordx4 v[24:27], v208, s[64:65]
	v_mfma_scale_f32_16x16x128_f8f6f4 v[100:103], v[148:151], v[152:159], v[100:103], v215, v215 op_sel_hi:[0,0,0] cbsz:4
	ds_write_b128 v110, v[44:47] offset:432
	v_bfe_u32 v209, v227, 16, 16
	v_lshl_or_b32 v209, v209, 7, v113
	global_load_dwordx4 v[28:31], v209, s[64:65]
	s_lshl_b32 s78, s2, 10
	s_add_i32 s78, s78, 64
	v_add_u32_e32 v120, s78, v114
	v_mov_b32_e32 v121, 0x1a000
	v_cndmask_b32_e64 v122, v121, v120, s[30:31]
	v_cndmask_b32_e64 v121, v121, v120, s[44:45]
	ds_read_b128 v[80:83], v122
	ds_read_b128 v[84:87], v121
	s_lshl_b32 s78, s33, 8
	v_add_u32_e32 v123, s78, v112
	ds_read_b64 v[108:109], v123 offset:128
	ds_read_b64_tr_b4 v[64:65], v111 offset:0
	ds_read_b64_tr_b4 v[66:67], v111 offset:2304
	ds_read_b64_tr_b4 v[68:69], v111 offset:32
	ds_read_b64_tr_b4 v[70:71], v111 offset:2336
	ds_read_b64_tr_b4 v[72:73], v111 offset:64
	ds_read_b64_tr_b4 v[74:75], v111 offset:2368
	ds_read_b64_tr_b4 v[76:77], v111 offset:96
	ds_read_b64_tr_b4 v[78:79], v111 offset:2400
	s_waitcnt lgkmcnt(0)
	s_waitcnt vmcnt(9)
	v_mfma_scale_f32_16x16x128_f8f6f4 v[88:91], v[64:67], v[80:87], v[88:91], v215, v215 op_sel_hi:[0,0,0] cbsz:4
	ds_write_b128 v110, v[48:51] offset:0
	v_lshlrev_b32_e32 v208, 7, v108
	v_and_or_b32 v208, v208, s77, v113
	global_load_dwordx4 v[32:35], v208, s[64:65]
	v_mfma_scale_f32_16x16x128_f8f6f4 v[92:95], v[68:71], v[80:87], v[92:95], v215, v215 op_sel_hi:[0,0,0] cbsz:4
	ds_write_b128 v110, v[52:55] offset:144
	v_bfe_u32 v209, v108, 16, 16
	v_lshl_or_b32 v209, v209, 7, v113
	global_load_dwordx4 v[36:39], v209, s[64:65]
	v_mfma_scale_f32_16x16x128_f8f6f4 v[96:99], v[72:75], v[80:87], v[96:99], v215, v215 op_sel_hi:[0,0,0] cbsz:4
	ds_write_b128 v110, v[56:59] offset:288
	v_lshlrev_b32_e32 v208, 7, v109
	v_and_or_b32 v208, v208, s77, v113
	global_load_dwordx4 v[40:43], v208, s[64:65]
	v_mfma_scale_f32_16x16x128_f8f6f4 v[100:103], v[76:79], v[80:87], v[100:103], v215, v215 op_sel_hi:[0,0,0] cbsz:4
	ds_write_b128 v110, v[60:63] offset:432
	v_bfe_u32 v209, v109, 16, 16
	v_lshl_or_b32 v209, v209, 7, v113
	global_load_dwordx4 v[44:47], v209, s[64:65]
	s_lshl_b32 s78, s2, 10
	s_add_i32 s78, s78, 96
	v_add_u32_e32 v120, s78, v114
	v_mov_b32_e32 v121, 0x1a000
	v_cndmask_b32_e64 v122, v121, v120, s[30:31]
	v_cndmask_b32_e64 v121, v121, v120, s[44:45]
	ds_read_b128 v[152:155], v122
	ds_read_b128 v[156:159], v121
	s_lshl_b32 s78, s33, 8
	v_add_u32_e32 v123, s78, v112
	ds_read_b64 v[226:227], v123 offset:192
	ds_read_b64_tr_b4 v[136:137], v111 offset:0
	ds_read_b64_tr_b4 v[138:139], v111 offset:2304
	ds_read_b64_tr_b4 v[140:141], v111 offset:32
	ds_read_b64_tr_b4 v[142:143], v111 offset:2336
	ds_read_b64_tr_b4 v[144:145], v111 offset:64
	ds_read_b64_tr_b4 v[146:147], v111 offset:2368
	ds_read_b64_tr_b4 v[148:149], v111 offset:96
	ds_read_b64_tr_b4 v[150:151], v111 offset:2400
	s_waitcnt lgkmcnt(0)
; __device__ __forceinline__ unsigned pk2(float lo, float hi) { return f2bf(lo) | (f2bf(hi) << 16); }
; __device__ __forceinline__ void expert_phase(const Frame& F, int l, int xcc, LAS unsigned char* wl, const LAS unsigned char* zb) {
;     ...
;                 unsigned o2[2];
;                 {
;                     const bool b5 = (lane & 32) != 0, b4 = (lane & 16) != 0, b3 = (lane & 8) != 0;
;                     unsigned q8[8], q4[4];
;                     auto hadd = [](unsigned x, unsigned y) { return __builtin_bit_cast(unsigned, __builtin_bit_cast(hf2, x) + __builtin_bit_cast(hf2, y)); };
; #pragma unroll
;                     for (int n = 0; n < 8; ++n) { const unsigned send = b5 ? out[n] : out[n + 8], keep = b5 ? out[n + 8] : out[n]; q8[n] = hadd(keep, (unsigned)__shfl_xor((int)send, 32)); }
; #pragma unroll
;                     for (int n = 0; n < 4; ++n) { const unsigned send = b4 ? q8[n] : q8[n + 4], keep = b4 ? q8[n + 4] : q8[n]; q4[n] = hadd(keep, (unsigned)__shfl_xor((int)send, 16)); }
; #pragma unroll
;                     for (int n = 0; n < 2; ++n) { const unsigned send = b3 ? q4[n] : q4[n + 2], keep = b3 ? q4[n + 2] : q4[n]; o2[n] = hadd(keep, (unsigned)__shfl_xor((int)send, 8)); }
;                 }
;                 const float isc = RS[8 + k];
;                 const hf2 oa = __builtin_bit_cast(hf2, o2[0]), ob = __builtin_bit_cast(hf2, o2[1]);
;                 const float y0 = bf_lo(xw.x) + (float)oa[0] * isc, y1 = bf_hi(xw.x) + (float)oa[1] * isc, y2 = bf_lo(xw.y) + (float)ob[0] * isc, y3 = bf_hi(xw.y) + (float)ob[1] * isc;
;                 if (l + 1 < DEPTH) {
;                     u32x2 w; w.x = pk2(y0, y1); w.y = pk2(y2, y3);
;                     sto_u2(XR + (size_t)t * D + sl * 256, 2u * col, w);
;                     const float s = (y0 * y0 + y1 * y1) + (y2 * y2 + y3 * y3);
;                     (void)__hip_atomic_fetch_add(SQ + k * 64 + lane, s, __ATOMIC_RELAXED, __HIP_MEMORY_SCOPE_WAVEFRONT);
;                 } else sto_f4(F.out + (size_t)t * D + sl * 256, 4u * col, (f32x4){y0, y1, y2, y3});
	v_mfma_scale_f32_16x16x128_f8f6f4 v[88:91], v[136:139], v[152:159], v[88:91], v215, v215 op_sel_hi:[0,0,0] cbsz:4
	v_lshlrev_b32_e32 v208, 7, v226
	v_and_or_b32 v208, v208, s77, v113
	global_load_dwordx4 v[48:51], v208, s[64:65]
	v_mfma_scale_f32_16x16x128_f8f6f4 v[92:95], v[140:143], v[152:159], v[92:95], v215, v215 op_sel_hi:[0,0,0] cbsz:4
	v_bfe_u32 v209, v226, 16, 16
	v_lshl_or_b32 v209, v209, 7, v113
	global_load_dwordx4 v[52:55], v209, s[64:65]
	v_mfma_scale_f32_16x16x128_f8f6f4 v[96:99], v[144:147], v[152:159], v[96:99], v215, v215 op_sel_hi:[0,0,0] cbsz:4
	v_lshlrev_b32_e32 v208, 7, v227
	v_and_or_b32 v208, v208, s77, v113
	global_load_dwordx4 v[56:59], v208, s[64:65]
	v_mfma_scale_f32_16x16x128_f8f6f4 v[100:103], v[148:151], v[152:159], v[100:103], v215, v215 op_sel_hi:[0,0,0] cbsz:4
	v_bfe_u32 v209, v227, 16, 16
	v_lshl_or_b32 v209, v209, 7, v113
	global_load_dwordx4 v[60:63], v209, s[64:65]
	s_add_i32 s4, s67, 2
	s_min_i32 s4, s4, 63
	s_and_b32 s5, s4, 7
	s_waitcnt vmcnt(12)
	ds_write_b128 v110, v[0:3] offset:0
	ds_write_b128 v110, v[4:7] offset:144
	ds_write_b128 v110, v[8:11] offset:288
	ds_write_b128 v110, v[12:15] offset:432
	s_lshl_b32 s78, s33, 10
	v_add_u32_e32 v120, s78, v114
	v_mov_b32_e32 v121, 0x1a000
	v_cndmask_b32_e64 v122, v121, v120, s[30:31]
	v_cndmask_b32_e64 v121, v121, v120, s[44:45]
	ds_read_b128 v[80:83], v122
	ds_read_b128 v[84:87], v121
	s_lshl_b32 s78, s5, 8
	v_add_u32_e32 v123, s78, v112
	ds_read_b64 v[108:109], v123 offset:0
	ds_read_b64_tr_b4 v[64:65], v111 offset:0
	ds_read_b64_tr_b4 v[66:67], v111 offset:2304
	ds_read_b64_tr_b4 v[68:69], v111 offset:32
	ds_read_b64_tr_b4 v[70:71], v111 offset:2336
	ds_read_b64_tr_b4 v[72:73], v111 offset:64
	ds_read_b64_tr_b4 v[74:75], v111 offset:2368
	ds_read_b64_tr_b4 v[76:77], v111 offset:96
	ds_read_b64_tr_b4 v[78:79], v111 offset:2400
	s_ashr_i32 s55, s8, 31
	s_mov_b32 s54, s8
	s_lshl_b64 s[54:55], s[54:55], 12
	s_lshl_b32 s78, s3, 9
	s_add_u32 s4, s48, s54
	s_addc_u32 s5, s49, s55
	s_add_u32 s4, s4, s78
	s_addc_u32 s5, s5, 0
	s_lshl_b32 s78, s2, 2
	s_add_i32 s78, s78, s83
	v_mov_b32_e32 v120, s78
	s_lshl_b32 s78, s2, 8
	v_add_u32_e32 v121, s78, v117
	ds_read_b32 v122, v120 offset:10272
	ds_read_b32 v123, v121
	v_add_f32_dpp v88, v88, v88 row_shl:4 row_mask:0xf bank_mask:0xf
	v_add_f32_dpp v89, v89, v89 row_shl:4 row_mask:0xf bank_mask:0xf
	v_add_f32_dpp v90, v90, v90 row_shl:4 row_mask:0xf bank_mask:0xf
	v_add_f32_dpp v91, v91, v91 row_shl:4 row_mask:0xf bank_mask:0xf
	v_add_f32_dpp v92, v92, v92 row_shl:4 row_mask:0xf bank_mask:0xf
	v_add_f32_dpp v93, v93, v93 row_shl:4 row_mask:0xf bank_mask:0xf
	v_add_f32_dpp v94, v94, v94 row_shl:4 row_mask:0xf bank_mask:0xf
	v_add_f32_dpp v95, v95, v95 row_shl:4 row_mask:0xf bank_mask:0xf
	v_add_f32_dpp v96, v96, v96 row_shl:4 row_mask:0xf bank_mask:0xf
	v_add_f32_dpp v97, v97, v97 row_shl:4 row_mask:0xf bank_mask:0xf
	v_add_f32_dpp v98, v98, v98 row_shl:4 row_mask:0xf bank_mask:0xf
	v_add_f32_dpp v99, v99, v99 row_shl:4 row_mask:0xf bank_mask:0xf
	v_add_f32_dpp v100, v100, v100 row_shl:4 row_mask:0xf bank_mask:0xf
	v_add_f32_dpp v101, v101, v101 row_shl:4 row_mask:0xf bank_mask:0xf
	v_add_f32_dpp v102, v102, v102 row_shl:4 row_mask:0xf bank_mask:0xf
	v_add_f32_dpp v103, v103, v103 row_shl:4 row_mask:0xf bank_mask:0xf
	v_add_f32_dpp v88, v88, v88 row_shl:8 row_mask:0xf bank_mask:0xf
	v_add_f32_dpp v89, v89, v89 row_shl:8 row_mask:0xf bank_mask:0xf
	v_add_f32_dpp v90, v90, v90 row_shl:8 row_mask:0xf bank_mask:0xf
	v_add_f32_dpp v91, v91, v91 row_shl:8 row_mask:0xf bank_mask:0xf
	v_add_f32_dpp v92, v92, v92 row_shl:8 row_mask:0xf bank_mask:0xf
	v_add_f32_dpp v93, v93, v93 row_shl:8 row_mask:0xf bank_mask:0xf
	v_add_f32_dpp v94, v94, v94 row_shl:8 row_mask:0xf bank_mask:0xf
	v_add_f32_dpp v95, v95, v95 row_shl:8 row_mask:0xf bank_mask:0xf
	v_add_f32_dpp v96, v96, v96 row_shl:8 row_mask:0xf bank_mask:0xf
	v_add_f32_dpp v97, v97, v97 row_shl:8 row_mask:0xf bank_mask:0xf
	v_add_f32_dpp v98, v98, v98 row_shl:8 row_mask:0xf bank_mask:0xf
	v_add_f32_dpp v99, v99, v99 row_shl:8 row_mask:0xf bank_mask:0xf
	v_add_f32_dpp v100, v100, v100 row_shl:8 row_mask:0xf bank_mask:0xf
	v_add_f32_dpp v101, v101, v101 row_shl:8 row_mask:0xf bank_mask:0xf
	v_add_f32_dpp v102, v102, v102 row_shl:8 row_mask:0xf bank_mask:0xf
	v_add_f32_dpp v103, v103, v103 row_shl:8 row_mask:0xf bank_mask:0xf
	s_mov_b64 exec, s[100:101]
	ds_write_b128 v115, v[88:91] offset:0
	ds_write_b128 v115, v[92:95] offset:1024
	ds_write_b128 v115, v[96:99] offset:2048
	ds_write_b128 v115, v[100:103] offset:3072
	s_mov_b64 exec, -1
	ds_read_b128 v[104:107], v116
	s_waitcnt vmcnt(16) lgkmcnt(0)
	v_lshlrev_b32_e32 v124, 16, v172
	v_and_b32_e32 v125, 0xffff0000, v172
	v_lshlrev_b32_e32 v126, 16, v173
	v_and_b32_e32 v127, 0xffff0000, v173
	v_fma_f32 v124, v104, v122, v124
	v_fma_f32 v125, v105, v122, v125
	v_fma_f32 v126, v106, v122, v126
	v_fma_f32 v127, v107, v122, v127
	s_ashr_i32 s55, s9, 31
	s_mov_b32 s54, s9
	s_lshl_b64 s[54:55], s[54:55], 12
	s_add_u32 s54, s90, s54
	s_addc_u32 s55, s91, s55
	s_lshl_b32 s78, s58, 9
	s_add_u32 s54, s54, s78
	s_addc_u32 s55, s55, 0
	v_lshl_add_u64 v[208:209], s[54:55], 0, v[184:185]
	global_load_dwordx2 v[172:173], v[208:209], off
	s_and_b64 vcc, exec, s[20:21]
	s_cbranch_vccz .Lv_last
	v_bfe_u32 v128, v124, 16, 1
	v_bfe_u32 v129, v125, 16, 1
	v_bfe_u32 v130, v126, 16, 1
	v_bfe_u32 v131, v127, 16, 1
	v_add3_u32 v128, v124, v128, s68
	v_add3_u32 v129, v125, v129, s68
	v_add3_u32 v130, v126, v130, s68
	v_add3_u32 v131, v127, v131, s68
	v_perm_b32 v132, v129, v128, s66
	v_perm_b32 v133, v131, v130, s66
	v_lshl_add_u64 v[208:209], s[4:5], 0, v[184:185]
	global_store_dwordx2 v[208:209], v[132:133], off
	v_mul_f32_e32 v134, v124, v124
	v_fmac_f32_e32 v134, v125, v125
	v_fmac_f32_e32 v134, v126, v126
	v_fmac_f32_e32 v134, v127, v127
	v_add_f32_e32 v123, v123, v134
	ds_write_b32 v121, v123
	s_branch .Lv_next
